# projection GEMM epilogues: non-temporal loads for the read-once gate and residual rows
# baseline (speedup 1.0000x reference)
.LBB0_1132:
	v_lshl_add_u32 v150, s26, 8, v158
	v_lshl_or_b32 v148, s51, 8, v163
	v_mov_b64_e32 v[152:153], s[96:97]
	v_ashrrev_i32_e32 v149, 31, v148
	v_lshlrev_b64 v[146:147], 1, v[148:149]
	v_or_b32_e32 v148, 0x80, v148
	v_ashrrev_i32_e32 v149, 31, v148
	v_lshlrev_b64 v[148:149], 1, v[148:149]
	v_mov_b32_e32 v168, v150
	v_mad_i64_i32 v[172:173], s[0:1], v168, s50, v[152:153]
	v_lshl_add_u64 v[172:173], v[172:173], 0, s[16:17]
	v_lshl_add_u64 v[174:175], v[172:173], 0, v[146:147]
	global_load_dwordx4 v[176:179], v[174:175], off nt
	v_lshl_add_u64 v[174:175], v[172:173], 0, v[148:149]
	global_load_dwordx4 v[180:183], v[174:175], off nt
	v_or_b32_e32 v168, 16, v150
	v_mad_i64_i32 v[172:173], s[0:1], v168, s50, v[152:153]
	v_lshl_add_u64 v[172:173], v[172:173], 0, s[16:17]
	v_lshl_add_u64 v[174:175], v[172:173], 0, v[146:147]
	global_load_dwordx4 v[184:187], v[174:175], off nt
	v_lshl_add_u64 v[174:175], v[172:173], 0, v[148:149]
	global_load_dwordx4 v[188:191], v[174:175], off nt
	v_or_b32_e32 v168, 32, v150
	v_mad_i64_i32 v[172:173], s[0:1], v168, s50, v[152:153]
	v_lshl_add_u64 v[172:173], v[172:173], 0, s[16:17]
	v_lshl_add_u64 v[174:175], v[172:173], 0, v[146:147]
	global_load_dwordx4 v[192:195], v[174:175], off nt
	v_lshl_add_u64 v[174:175], v[172:173], 0, v[148:149]
	global_load_dwordx4 v[196:199], v[174:175], off nt
	v_or_b32_e32 v168, 48, v150
	v_mad_i64_i32 v[172:173], s[0:1], v168, s50, v[152:153]
	v_lshl_add_u64 v[172:173], v[172:173], 0, s[16:17]
	v_lshl_add_u64 v[174:175], v[172:173], 0, v[146:147]
	global_load_dwordx4 v[200:203], v[174:175], off nt
	v_lshl_add_u64 v[174:175], v[172:173], 0, v[148:149]
	global_load_dwordx4 v[204:207], v[174:175], off nt
	v_or_b32_e32 v168, 128, v150
	v_mad_i64_i32 v[172:173], s[0:1], v168, s50, v[152:153]
	v_lshl_add_u64 v[172:173], v[172:173], 0, s[16:17]
	v_lshl_add_u64 v[174:175], v[172:173], 0, v[146:147]
	global_load_dwordx4 v[208:211], v[174:175], off nt
	v_lshl_add_u64 v[174:175], v[172:173], 0, v[148:149]
	global_load_dwordx4 v[212:215], v[174:175], off nt
	v_or_b32_e32 v168, 144, v150
	v_mad_i64_i32 v[172:173], s[0:1], v168, s50, v[152:153]
	v_lshl_add_u64 v[172:173], v[172:173], 0, s[16:17]
	v_lshl_add_u64 v[174:175], v[172:173], 0, v[146:147]
	global_load_dwordx4 v[216:219], v[174:175], off nt
	v_lshl_add_u64 v[174:175], v[172:173], 0, v[148:149]
	global_load_dwordx4 v[220:223], v[174:175], off nt
	v_or_b32_e32 v168, 160, v150
	v_mad_i64_i32 v[172:173], s[0:1], v168, s50, v[152:153]
	v_lshl_add_u64 v[172:173], v[172:173], 0, s[16:17]
	v_lshl_add_u64 v[174:175], v[172:173], 0, v[146:147]
	global_load_dwordx4 v[224:227], v[174:175], off nt
	v_lshl_add_u64 v[174:175], v[172:173], 0, v[148:149]
	global_load_dwordx4 v[228:231], v[174:175], off nt
	v_or_b32_e32 v168, 176, v150
	v_mad_i64_i32 v[172:173], s[0:1], v168, s50, v[152:153]
	v_lshl_add_u64 v[172:173], v[172:173], 0, s[16:17]
	v_lshl_add_u64 v[174:175], v[172:173], 0, v[146:147]
	global_load_dwordx4 v[232:235], v[174:175], off nt
	v_lshl_add_u64 v[174:175], v[172:173], 0, v[148:149]
	global_load_dwordx4 v[236:239], v[174:175], off nt
	s_waitcnt vmcnt(15)
	v_lshlrev_b32_e32 v0, 16, v176
	v_and_b32_e32 v151, 0xffff0000, v176
	v_lshlrev_b32_e32 v167, 16, v177
	v_and_b32_e32 v169, 0xffff0000, v177
	v_lshlrev_b32_e32 v170, 16, v178
	v_and_b32_e32 v171, 0xffff0000, v178
	v_lshlrev_b32_e32 v174, 16, v179
	v_and_b32_e32 v175, 0xffff0000, v179
	v_mul_f32_e32 v0, 0xbfb8aa3b, v0
	v_mul_f32_e32 v151, 0xbfb8aa3b, v151
	v_mul_f32_e32 v167, 0xbfb8aa3b, v167
	v_mul_f32_e32 v169, 0xbfb8aa3b, v169
	v_mul_f32_e32 v170, 0xbfb8aa3b, v170
	v_mul_f32_e32 v171, 0xbfb8aa3b, v171
	v_mul_f32_e32 v174, 0xbfb8aa3b, v174
	v_mul_f32_e32 v175, 0xbfb8aa3b, v175
	v_exp_f32_e32 v0, v0
	v_exp_f32_e32 v151, v151
	v_exp_f32_e32 v167, v167
	v_exp_f32_e32 v169, v169
	v_exp_f32_e32 v170, v170
	v_exp_f32_e32 v171, v171
	v_exp_f32_e32 v174, v174
	v_exp_f32_e32 v175, v175
	v_add_f32_e32 v0, 1.0, v0
	v_add_f32_e32 v151, 1.0, v151
	v_add_f32_e32 v167, 1.0, v167
	v_add_f32_e32 v169, 1.0, v169
	v_add_f32_e32 v170, 1.0, v170
	v_add_f32_e32 v171, 1.0, v171
	v_add_f32_e32 v174, 1.0, v174
	v_add_f32_e32 v175, 1.0, v175
	v_rcp_f32_e32 v0, v0
	v_rcp_f32_e32 v151, v151
	v_rcp_f32_e32 v167, v167
	v_rcp_f32_e32 v169, v169
	v_rcp_f32_e32 v170, v170
	v_rcp_f32_e32 v171, v171
	v_rcp_f32_e32 v174, v174
	v_rcp_f32_e32 v175, v175
	v_mul_f32_e32 v0, v126, v0
	v_mul_f32_e32 v151, v127, v151
	v_mul_f32_e32 v167, v128, v167
	v_mul_f32_e32 v169, v129, v169
	v_mul_f32_e32 v170, v122, v170
	v_mul_f32_e32 v171, v123, v171
	v_mul_f32_e32 v174, v124, v174
	v_mul_f32_e32 v175, v125, v175
	v_cvt_pk_bf16_f32 v126, v0, v151
	v_cvt_pk_bf16_f32 v127, v167, v169
	v_cvt_pk_bf16_f32 v128, v170, v171
	v_cvt_pk_bf16_f32 v129, v174, v175
	v_mov_b32_e32 v172, v150
	v_mov_b32_e32 v173, 0
	v_lshlrev_b64 v[172:173], 12, v[172:173]
	v_lshl_add_u64 v[172:173], s[6:7], 0, v[172:173]
	v_lshl_add_u64 v[172:173], v[172:173], 0, v[146:147]
	global_store_dwordx4 v[172:173], v[126:129], off
	s_waitcnt vmcnt(15)
	v_lshlrev_b32_e32 v0, 16, v180
	v_and_b32_e32 v151, 0xffff0000, v180
	v_lshlrev_b32_e32 v167, 16, v181
	v_and_b32_e32 v169, 0xffff0000, v181
	v_lshlrev_b32_e32 v170, 16, v182
	v_and_b32_e32 v171, 0xffff0000, v182
	v_lshlrev_b32_e32 v174, 16, v183
	v_and_b32_e32 v175, 0xffff0000, v183
	v_mul_f32_e32 v0, 0xbfb8aa3b, v0
	v_mul_f32_e32 v151, 0xbfb8aa3b, v151
	v_mul_f32_e32 v167, 0xbfb8aa3b, v167
	v_mul_f32_e32 v169, 0xbfb8aa3b, v169
	v_mul_f32_e32 v170, 0xbfb8aa3b, v170
	v_mul_f32_e32 v171, 0xbfb8aa3b, v171
	v_mul_f32_e32 v174, 0xbfb8aa3b, v174
	v_mul_f32_e32 v175, 0xbfb8aa3b, v175
	v_exp_f32_e32 v0, v0
	v_exp_f32_e32 v151, v151
	v_exp_f32_e32 v167, v167
	v_exp_f32_e32 v169, v169
	v_exp_f32_e32 v170, v170
	v_exp_f32_e32 v171, v171
	v_exp_f32_e32 v174, v174
	v_exp_f32_e32 v175, v175
	v_add_f32_e32 v0, 1.0, v0
	v_add_f32_e32 v151, 1.0, v151
	v_add_f32_e32 v167, 1.0, v167
	v_add_f32_e32 v169, 1.0, v169
	v_add_f32_e32 v170, 1.0, v170
	v_add_f32_e32 v171, 1.0, v171
	v_add_f32_e32 v174, 1.0, v174
	v_add_f32_e32 v175, 1.0, v175
	v_rcp_f32_e32 v0, v0
	v_rcp_f32_e32 v151, v151
	v_rcp_f32_e32 v167, v167
	v_rcp_f32_e32 v169, v169
	v_rcp_f32_e32 v170, v170
	v_rcp_f32_e32 v171, v171
	v_rcp_f32_e32 v174, v174
	v_rcp_f32_e32 v175, v175
	v_mul_f32_e32 v0, v118, v0
	v_mul_f32_e32 v151, v119, v151
	v_mul_f32_e32 v167, v120, v167
	v_mul_f32_e32 v169, v121, v169
	v_mul_f32_e32 v170, v114, v170
	v_mul_f32_e32 v171, v115, v171
	v_mul_f32_e32 v174, v116, v174
	v_mul_f32_e32 v175, v117, v175
	v_cvt_pk_bf16_f32 v118, v0, v151
	v_cvt_pk_bf16_f32 v119, v167, v169
	v_cvt_pk_bf16_f32 v120, v170, v171
	v_cvt_pk_bf16_f32 v121, v174, v175
	global_store_dwordx4 v[172:173], v[118:121], off offset:256
	s_waitcnt vmcnt(15)
	v_lshlrev_b32_e32 v0, 16, v184
	v_and_b32_e32 v151, 0xffff0000, v184
	v_lshlrev_b32_e32 v167, 16, v185
	v_and_b32_e32 v169, 0xffff0000, v185
	v_lshlrev_b32_e32 v170, 16, v186
	v_and_b32_e32 v171, 0xffff0000, v186
	v_lshlrev_b32_e32 v174, 16, v187
	v_and_b32_e32 v175, 0xffff0000, v187
	v_mul_f32_e32 v0, 0xbfb8aa3b, v0
	v_mul_f32_e32 v151, 0xbfb8aa3b, v151
	v_mul_f32_e32 v167, 0xbfb8aa3b, v167
	v_mul_f32_e32 v169, 0xbfb8aa3b, v169
	v_mul_f32_e32 v170, 0xbfb8aa3b, v170
	v_mul_f32_e32 v171, 0xbfb8aa3b, v171
	v_mul_f32_e32 v174, 0xbfb8aa3b, v174
	v_mul_f32_e32 v175, 0xbfb8aa3b, v175
	v_exp_f32_e32 v0, v0
	v_exp_f32_e32 v151, v151
	v_exp_f32_e32 v167, v167
	v_exp_f32_e32 v169, v169
	v_exp_f32_e32 v170, v170
	v_exp_f32_e32 v171, v171
	v_exp_f32_e32 v174, v174
	v_exp_f32_e32 v175, v175
	v_add_f32_e32 v0, 1.0, v0
	v_add_f32_e32 v151, 1.0, v151
	v_add_f32_e32 v167, 1.0, v167
	v_add_f32_e32 v169, 1.0, v169
	v_add_f32_e32 v170, 1.0, v170
	v_add_f32_e32 v171, 1.0, v171
	v_add_f32_e32 v174, 1.0, v174
	v_add_f32_e32 v175, 1.0, v175
	v_rcp_f32_e32 v0, v0
	v_rcp_f32_e32 v151, v151
	v_rcp_f32_e32 v167, v167
	v_rcp_f32_e32 v169, v169
	v_rcp_f32_e32 v170, v170
	v_rcp_f32_e32 v171, v171
	v_rcp_f32_e32 v174, v174
	v_rcp_f32_e32 v175, v175
	v_mul_f32_e32 v0, v110, v0
	v_mul_f32_e32 v151, v111, v151
	v_mul_f32_e32 v167, v112, v167
	v_mul_f32_e32 v169, v113, v169
	v_mul_f32_e32 v170, v106, v170
	v_mul_f32_e32 v171, v107, v171
	v_mul_f32_e32 v174, v108, v174
	v_mul_f32_e32 v175, v109, v175
	v_cvt_pk_bf16_f32 v110, v0, v151
	v_cvt_pk_bf16_f32 v111, v167, v169
	v_cvt_pk_bf16_f32 v112, v170, v171
	v_cvt_pk_bf16_f32 v113, v174, v175
	v_or_b32_e32 v172, 16, v150
	v_mov_b32_e32 v173, 0
	v_lshlrev_b64 v[172:173], 12, v[172:173]
	v_lshl_add_u64 v[172:173], s[6:7], 0, v[172:173]
	v_lshl_add_u64 v[172:173], v[172:173], 0, v[146:147]
	global_store_dwordx4 v[172:173], v[110:113], off
	s_waitcnt vmcnt(15)
	v_lshlrev_b32_e32 v0, 16, v188
	v_and_b32_e32 v151, 0xffff0000, v188
	v_lshlrev_b32_e32 v167, 16, v189
	v_and_b32_e32 v169, 0xffff0000, v189
	v_lshlrev_b32_e32 v170, 16, v190
	v_and_b32_e32 v171, 0xffff0000, v190
	v_lshlrev_b32_e32 v174, 16, v191
	v_and_b32_e32 v175, 0xffff0000, v191
	v_mul_f32_e32 v0, 0xbfb8aa3b, v0
	v_mul_f32_e32 v151, 0xbfb8aa3b, v151
	v_mul_f32_e32 v167, 0xbfb8aa3b, v167
	v_mul_f32_e32 v169, 0xbfb8aa3b, v169
	v_mul_f32_e32 v170, 0xbfb8aa3b, v170
	v_mul_f32_e32 v171, 0xbfb8aa3b, v171
	v_mul_f32_e32 v174, 0xbfb8aa3b, v174
	v_mul_f32_e32 v175, 0xbfb8aa3b, v175
	v_exp_f32_e32 v0, v0
	v_exp_f32_e32 v151, v151
	v_exp_f32_e32 v167, v167
	v_exp_f32_e32 v169, v169
	v_exp_f32_e32 v170, v170
	v_exp_f32_e32 v171, v171
	v_exp_f32_e32 v174, v174
	v_exp_f32_e32 v175, v175
	v_add_f32_e32 v0, 1.0, v0
	v_add_f32_e32 v151, 1.0, v151
	v_add_f32_e32 v167, 1.0, v167
	v_add_f32_e32 v169, 1.0, v169
	v_add_f32_e32 v170, 1.0, v170
	v_add_f32_e32 v171, 1.0, v171
	v_add_f32_e32 v174, 1.0, v174
	v_add_f32_e32 v175, 1.0, v175
	v_rcp_f32_e32 v0, v0
	v_rcp_f32_e32 v151, v151
	v_rcp_f32_e32 v167, v167
	v_rcp_f32_e32 v169, v169
	v_rcp_f32_e32 v170, v170
	v_rcp_f32_e32 v171, v171
	v_rcp_f32_e32 v174, v174
	v_rcp_f32_e32 v175, v175
	v_mul_f32_e32 v0, v102, v0
	v_mul_f32_e32 v151, v103, v151
	v_mul_f32_e32 v167, v104, v167
	v_mul_f32_e32 v169, v105, v169
	v_mul_f32_e32 v170, v98, v170
	v_mul_f32_e32 v171, v99, v171
	v_mul_f32_e32 v174, v100, v174
	v_mul_f32_e32 v175, v101, v175
	v_cvt_pk_bf16_f32 v102, v0, v151
	v_cvt_pk_bf16_f32 v103, v167, v169
	v_cvt_pk_bf16_f32 v104, v170, v171
	v_cvt_pk_bf16_f32 v105, v174, v175
	global_store_dwordx4 v[172:173], v[102:105], off offset:256
	s_waitcnt vmcnt(15)
	v_lshlrev_b32_e32 v0, 16, v192
	v_and_b32_e32 v151, 0xffff0000, v192
	v_lshlrev_b32_e32 v167, 16, v193
	v_and_b32_e32 v169, 0xffff0000, v193
	v_lshlrev_b32_e32 v170, 16, v194
	v_and_b32_e32 v171, 0xffff0000, v194
	v_lshlrev_b32_e32 v174, 16, v195
	v_and_b32_e32 v175, 0xffff0000, v195
	v_mul_f32_e32 v0, 0xbfb8aa3b, v0
	v_mul_f32_e32 v151, 0xbfb8aa3b, v151
	v_mul_f32_e32 v167, 0xbfb8aa3b, v167
	v_mul_f32_e32 v169, 0xbfb8aa3b, v169
	v_mul_f32_e32 v170, 0xbfb8aa3b, v170
	v_mul_f32_e32 v171, 0xbfb8aa3b, v171
	v_mul_f32_e32 v174, 0xbfb8aa3b, v174
	v_mul_f32_e32 v175, 0xbfb8aa3b, v175
	v_exp_f32_e32 v0, v0
	v_exp_f32_e32 v151, v151
	v_exp_f32_e32 v167, v167
	v_exp_f32_e32 v169, v169
	v_exp_f32_e32 v170, v170
	v_exp_f32_e32 v171, v171
	v_exp_f32_e32 v174, v174
	v_exp_f32_e32 v175, v175
	v_add_f32_e32 v0, 1.0, v0
	v_add_f32_e32 v151, 1.0, v151
	v_add_f32_e32 v167, 1.0, v167
	v_add_f32_e32 v169, 1.0, v169
	v_add_f32_e32 v170, 1.0, v170
	v_add_f32_e32 v171, 1.0, v171
	v_add_f32_e32 v174, 1.0, v174
	v_add_f32_e32 v175, 1.0, v175
	v_rcp_f32_e32 v0, v0
	v_rcp_f32_e32 v151, v151
	v_rcp_f32_e32 v167, v167
	v_rcp_f32_e32 v169, v169
	v_rcp_f32_e32 v170, v170
	v_rcp_f32_e32 v171, v171
	v_rcp_f32_e32 v174, v174
	v_rcp_f32_e32 v175, v175
	v_mul_f32_e32 v0, v94, v0
	v_mul_f32_e32 v151, v95, v151
	v_mul_f32_e32 v167, v96, v167
	v_mul_f32_e32 v169, v97, v169
	v_mul_f32_e32 v170, v90, v170
	v_mul_f32_e32 v171, v91, v171
	v_mul_f32_e32 v174, v92, v174
	v_mul_f32_e32 v175, v93, v175
	v_cvt_pk_bf16_f32 v94, v0, v151
	v_cvt_pk_bf16_f32 v95, v167, v169
	v_cvt_pk_bf16_f32 v96, v170, v171
	v_cvt_pk_bf16_f32 v97, v174, v175
	v_or_b32_e32 v172, 32, v150
	v_mov_b32_e32 v173, 0
	v_lshlrev_b64 v[172:173], 12, v[172:173]
	v_lshl_add_u64 v[172:173], s[6:7], 0, v[172:173]
	v_lshl_add_u64 v[172:173], v[172:173], 0, v[146:147]
	global_store_dwordx4 v[172:173], v[94:97], off
	s_waitcnt vmcnt(15)
	v_lshlrev_b32_e32 v0, 16, v196
	v_and_b32_e32 v151, 0xffff0000, v196
	v_lshlrev_b32_e32 v167, 16, v197
	v_and_b32_e32 v169, 0xffff0000, v197
	v_lshlrev_b32_e32 v170, 16, v198
	v_and_b32_e32 v171, 0xffff0000, v198
	v_lshlrev_b32_e32 v174, 16, v199
	v_and_b32_e32 v175, 0xffff0000, v199
	v_mul_f32_e32 v0, 0xbfb8aa3b, v0
	v_mul_f32_e32 v151, 0xbfb8aa3b, v151
	v_mul_f32_e32 v167, 0xbfb8aa3b, v167
	v_mul_f32_e32 v169, 0xbfb8aa3b, v169
	v_mul_f32_e32 v170, 0xbfb8aa3b, v170
	v_mul_f32_e32 v171, 0xbfb8aa3b, v171
	v_mul_f32_e32 v174, 0xbfb8aa3b, v174
	v_mul_f32_e32 v175, 0xbfb8aa3b, v175
	v_exp_f32_e32 v0, v0
	v_exp_f32_e32 v151, v151
	v_exp_f32_e32 v167, v167
	v_exp_f32_e32 v169, v169
	v_exp_f32_e32 v170, v170
	v_exp_f32_e32 v171, v171
	v_exp_f32_e32 v174, v174
	v_exp_f32_e32 v175, v175
	v_add_f32_e32 v0, 1.0, v0
	v_add_f32_e32 v151, 1.0, v151
	v_add_f32_e32 v167, 1.0, v167
	v_add_f32_e32 v169, 1.0, v169
	v_add_f32_e32 v170, 1.0, v170
	v_add_f32_e32 v171, 1.0, v171
	v_add_f32_e32 v174, 1.0, v174
	v_add_f32_e32 v175, 1.0, v175
	v_rcp_f32_e32 v0, v0
	v_rcp_f32_e32 v151, v151
	v_rcp_f32_e32 v167, v167
	v_rcp_f32_e32 v169, v169
	v_rcp_f32_e32 v170, v170
	v_rcp_f32_e32 v171, v171
	v_rcp_f32_e32 v174, v174
	v_rcp_f32_e32 v175, v175
	v_mul_f32_e32 v0, v86, v0
	v_mul_f32_e32 v151, v87, v151
	v_mul_f32_e32 v167, v88, v167
	v_mul_f32_e32 v169, v89, v169
	v_mul_f32_e32 v170, v82, v170
	v_mul_f32_e32 v171, v83, v171
	v_mul_f32_e32 v174, v84, v174
	v_mul_f32_e32 v175, v85, v175
	v_cvt_pk_bf16_f32 v86, v0, v151
	v_cvt_pk_bf16_f32 v87, v167, v169
	v_cvt_pk_bf16_f32 v88, v170, v171
	v_cvt_pk_bf16_f32 v89, v174, v175
	global_store_dwordx4 v[172:173], v[86:89], off offset:256
	s_waitcnt vmcnt(15)
	v_lshlrev_b32_e32 v0, 16, v200
	v_and_b32_e32 v151, 0xffff0000, v200
	v_lshlrev_b32_e32 v167, 16, v201
	v_and_b32_e32 v169, 0xffff0000, v201
	v_lshlrev_b32_e32 v170, 16, v202
	v_and_b32_e32 v171, 0xffff0000, v202
	v_lshlrev_b32_e32 v174, 16, v203
	v_and_b32_e32 v175, 0xffff0000, v203
	v_mul_f32_e32 v0, 0xbfb8aa3b, v0
	v_mul_f32_e32 v151, 0xbfb8aa3b, v151
	v_mul_f32_e32 v167, 0xbfb8aa3b, v167
	v_mul_f32_e32 v169, 0xbfb8aa3b, v169
	v_mul_f32_e32 v170, 0xbfb8aa3b, v170
	v_mul_f32_e32 v171, 0xbfb8aa3b, v171
	v_mul_f32_e32 v174, 0xbfb8aa3b, v174
	v_mul_f32_e32 v175, 0xbfb8aa3b, v175
	v_exp_f32_e32 v0, v0
	v_exp_f32_e32 v151, v151
	v_exp_f32_e32 v167, v167
	v_exp_f32_e32 v169, v169
	v_exp_f32_e32 v170, v170
	v_exp_f32_e32 v171, v171
	v_exp_f32_e32 v174, v174
	v_exp_f32_e32 v175, v175
	v_add_f32_e32 v0, 1.0, v0
	v_add_f32_e32 v151, 1.0, v151
	v_add_f32_e32 v167, 1.0, v167
	v_add_f32_e32 v169, 1.0, v169
	v_add_f32_e32 v170, 1.0, v170
	v_add_f32_e32 v171, 1.0, v171
	v_add_f32_e32 v174, 1.0, v174
	v_add_f32_e32 v175, 1.0, v175
	v_rcp_f32_e32 v0, v0
	v_rcp_f32_e32 v151, v151
	v_rcp_f32_e32 v167, v167
	v_rcp_f32_e32 v169, v169
	v_rcp_f32_e32 v170, v170
	v_rcp_f32_e32 v171, v171
	v_rcp_f32_e32 v174, v174
	v_rcp_f32_e32 v175, v175
	v_mul_f32_e32 v0, v78, v0
	v_mul_f32_e32 v151, v79, v151
	v_mul_f32_e32 v167, v80, v167
	v_mul_f32_e32 v169, v81, v169
	v_mul_f32_e32 v170, v74, v170
	v_mul_f32_e32 v171, v75, v171
	v_mul_f32_e32 v174, v76, v174
	v_mul_f32_e32 v175, v77, v175
	v_cvt_pk_bf16_f32 v78, v0, v151
	v_cvt_pk_bf16_f32 v79, v167, v169
	v_cvt_pk_bf16_f32 v80, v170, v171
	v_cvt_pk_bf16_f32 v81, v174, v175
	v_or_b32_e32 v172, 48, v150
	v_mov_b32_e32 v173, 0
	v_lshlrev_b64 v[172:173], 12, v[172:173]
	v_lshl_add_u64 v[172:173], s[6:7], 0, v[172:173]
	v_lshl_add_u64 v[172:173], v[172:173], 0, v[146:147]
	global_store_dwordx4 v[172:173], v[78:81], off
	s_waitcnt vmcnt(15)
	v_lshlrev_b32_e32 v0, 16, v204
	v_and_b32_e32 v151, 0xffff0000, v204
	v_lshlrev_b32_e32 v167, 16, v205
	v_and_b32_e32 v169, 0xffff0000, v205
	v_lshlrev_b32_e32 v170, 16, v206
	v_and_b32_e32 v171, 0xffff0000, v206
	v_lshlrev_b32_e32 v174, 16, v207
	v_and_b32_e32 v175, 0xffff0000, v207
	v_mul_f32_e32 v0, 0xbfb8aa3b, v0
	v_mul_f32_e32 v151, 0xbfb8aa3b, v151
	v_mul_f32_e32 v167, 0xbfb8aa3b, v167
	v_mul_f32_e32 v169, 0xbfb8aa3b, v169
	v_mul_f32_e32 v170, 0xbfb8aa3b, v170
	v_mul_f32_e32 v171, 0xbfb8aa3b, v171
	v_mul_f32_e32 v174, 0xbfb8aa3b, v174
	v_mul_f32_e32 v175, 0xbfb8aa3b, v175
	v_exp_f32_e32 v0, v0
	v_exp_f32_e32 v151, v151
	v_exp_f32_e32 v167, v167
	v_exp_f32_e32 v169, v169
	v_exp_f32_e32 v170, v170
	v_exp_f32_e32 v171, v171
	v_exp_f32_e32 v174, v174
	v_exp_f32_e32 v175, v175
	v_add_f32_e32 v0, 1.0, v0
	v_add_f32_e32 v151, 1.0, v151
	v_add_f32_e32 v167, 1.0, v167
	v_add_f32_e32 v169, 1.0, v169
	v_add_f32_e32 v170, 1.0, v170
	v_add_f32_e32 v171, 1.0, v171
	v_add_f32_e32 v174, 1.0, v174
	v_add_f32_e32 v175, 1.0, v175
	v_rcp_f32_e32 v0, v0
	v_rcp_f32_e32 v151, v151
	v_rcp_f32_e32 v167, v167
	v_rcp_f32_e32 v169, v169
	v_rcp_f32_e32 v170, v170
	v_rcp_f32_e32 v171, v171
	v_rcp_f32_e32 v174, v174
	v_rcp_f32_e32 v175, v175
	v_mul_f32_e32 v0, v70, v0
	v_mul_f32_e32 v151, v71, v151
	v_mul_f32_e32 v167, v72, v167
	v_mul_f32_e32 v169, v73, v169
	v_mul_f32_e32 v170, v66, v170
	v_mul_f32_e32 v171, v67, v171
	v_mul_f32_e32 v174, v68, v174
	v_mul_f32_e32 v175, v69, v175
	v_cvt_pk_bf16_f32 v70, v0, v151
	v_cvt_pk_bf16_f32 v71, v167, v169
	v_cvt_pk_bf16_f32 v72, v170, v171
	v_cvt_pk_bf16_f32 v73, v174, v175
	global_store_dwordx4 v[172:173], v[70:73], off offset:256
	s_waitcnt vmcnt(15)
	v_lshlrev_b32_e32 v0, 16, v208
	v_and_b32_e32 v151, 0xffff0000, v208
	v_lshlrev_b32_e32 v167, 16, v209
	v_and_b32_e32 v169, 0xffff0000, v209
	v_lshlrev_b32_e32 v170, 16, v210
	v_and_b32_e32 v171, 0xffff0000, v210
	v_lshlrev_b32_e32 v174, 16, v211
	v_and_b32_e32 v175, 0xffff0000, v211
	v_mul_f32_e32 v0, 0xbfb8aa3b, v0
	v_mul_f32_e32 v151, 0xbfb8aa3b, v151
	v_mul_f32_e32 v167, 0xbfb8aa3b, v167
	v_mul_f32_e32 v169, 0xbfb8aa3b, v169
	v_mul_f32_e32 v170, 0xbfb8aa3b, v170
	v_mul_f32_e32 v171, 0xbfb8aa3b, v171
	v_mul_f32_e32 v174, 0xbfb8aa3b, v174
	v_mul_f32_e32 v175, 0xbfb8aa3b, v175
	v_exp_f32_e32 v0, v0
	v_exp_f32_e32 v151, v151
	v_exp_f32_e32 v167, v167
	v_exp_f32_e32 v169, v169
	v_exp_f32_e32 v170, v170
	v_exp_f32_e32 v171, v171
	v_exp_f32_e32 v174, v174
	v_exp_f32_e32 v175, v175
	v_add_f32_e32 v0, 1.0, v0
	v_add_f32_e32 v151, 1.0, v151
	v_add_f32_e32 v167, 1.0, v167
	v_add_f32_e32 v169, 1.0, v169
	v_add_f32_e32 v170, 1.0, v170
	v_add_f32_e32 v171, 1.0, v171
	v_add_f32_e32 v174, 1.0, v174
	v_add_f32_e32 v175, 1.0, v175
	v_rcp_f32_e32 v0, v0
	v_rcp_f32_e32 v151, v151
	v_rcp_f32_e32 v167, v167
	v_rcp_f32_e32 v169, v169
	v_rcp_f32_e32 v170, v170
	v_rcp_f32_e32 v171, v171
	v_rcp_f32_e32 v174, v174
	v_rcp_f32_e32 v175, v175
	v_mul_f32_e32 v0, v62, v0
	v_mul_f32_e32 v151, v63, v151
	v_mul_f32_e32 v167, v64, v167
	v_mul_f32_e32 v169, v65, v169
	v_mul_f32_e32 v170, v58, v170
	v_mul_f32_e32 v171, v59, v171
	v_mul_f32_e32 v174, v60, v174
	v_mul_f32_e32 v175, v61, v175
	v_cvt_pk_bf16_f32 v62, v0, v151
	v_cvt_pk_bf16_f32 v63, v167, v169
	v_cvt_pk_bf16_f32 v64, v170, v171
	v_cvt_pk_bf16_f32 v65, v174, v175
	v_or_b32_e32 v172, 128, v150
	v_mov_b32_e32 v173, 0
	v_lshlrev_b64 v[172:173], 12, v[172:173]
	v_lshl_add_u64 v[172:173], s[6:7], 0, v[172:173]
	v_lshl_add_u64 v[172:173], v[172:173], 0, v[146:147]
	global_store_dwordx4 v[172:173], v[62:65], off
	s_waitcnt vmcnt(15)
	v_lshlrev_b32_e32 v0, 16, v212
	v_and_b32_e32 v151, 0xffff0000, v212
	v_lshlrev_b32_e32 v167, 16, v213
	v_and_b32_e32 v169, 0xffff0000, v213
	v_lshlrev_b32_e32 v170, 16, v214
	v_and_b32_e32 v171, 0xffff0000, v214
	v_lshlrev_b32_e32 v174, 16, v215
	v_and_b32_e32 v175, 0xffff0000, v215
	v_mul_f32_e32 v0, 0xbfb8aa3b, v0
	v_mul_f32_e32 v151, 0xbfb8aa3b, v151
	v_mul_f32_e32 v167, 0xbfb8aa3b, v167
	v_mul_f32_e32 v169, 0xbfb8aa3b, v169
	v_mul_f32_e32 v170, 0xbfb8aa3b, v170
	v_mul_f32_e32 v171, 0xbfb8aa3b, v171
	v_mul_f32_e32 v174, 0xbfb8aa3b, v174
	v_mul_f32_e32 v175, 0xbfb8aa3b, v175
	v_exp_f32_e32 v0, v0
	v_exp_f32_e32 v151, v151
	v_exp_f32_e32 v167, v167
	v_exp_f32_e32 v169, v169
	v_exp_f32_e32 v170, v170
	v_exp_f32_e32 v171, v171
	v_exp_f32_e32 v174, v174
	v_exp_f32_e32 v175, v175
	v_add_f32_e32 v0, 1.0, v0
	v_add_f32_e32 v151, 1.0, v151
	v_add_f32_e32 v167, 1.0, v167
	v_add_f32_e32 v169, 1.0, v169
	v_add_f32_e32 v170, 1.0, v170
	v_add_f32_e32 v171, 1.0, v171
	v_add_f32_e32 v174, 1.0, v174
	v_add_f32_e32 v175, 1.0, v175
	v_rcp_f32_e32 v0, v0
	v_rcp_f32_e32 v151, v151
	v_rcp_f32_e32 v167, v167
	v_rcp_f32_e32 v169, v169
	v_rcp_f32_e32 v170, v170
	v_rcp_f32_e32 v171, v171
	v_rcp_f32_e32 v174, v174
	v_rcp_f32_e32 v175, v175
	v_mul_f32_e32 v0, v54, v0
	v_mul_f32_e32 v151, v55, v151
	v_mul_f32_e32 v167, v56, v167
	v_mul_f32_e32 v169, v57, v169
	v_mul_f32_e32 v170, v50, v170
	v_mul_f32_e32 v171, v51, v171
	v_mul_f32_e32 v174, v52, v174
	v_mul_f32_e32 v175, v53, v175
	v_cvt_pk_bf16_f32 v54, v0, v151
	v_cvt_pk_bf16_f32 v55, v167, v169
	v_cvt_pk_bf16_f32 v56, v170, v171
	v_cvt_pk_bf16_f32 v57, v174, v175
	global_store_dwordx4 v[172:173], v[54:57], off offset:256
	s_waitcnt vmcnt(15)
	v_lshlrev_b32_e32 v0, 16, v216
	v_and_b32_e32 v151, 0xffff0000, v216
	v_lshlrev_b32_e32 v167, 16, v217
	v_and_b32_e32 v169, 0xffff0000, v217
	v_lshlrev_b32_e32 v170, 16, v218
	v_and_b32_e32 v171, 0xffff0000, v218
	v_lshlrev_b32_e32 v174, 16, v219
	v_and_b32_e32 v175, 0xffff0000, v219
	v_mul_f32_e32 v0, 0xbfb8aa3b, v0
	v_mul_f32_e32 v151, 0xbfb8aa3b, v151
	v_mul_f32_e32 v167, 0xbfb8aa3b, v167
	v_mul_f32_e32 v169, 0xbfb8aa3b, v169
	v_mul_f32_e32 v170, 0xbfb8aa3b, v170
	v_mul_f32_e32 v171, 0xbfb8aa3b, v171
	v_mul_f32_e32 v174, 0xbfb8aa3b, v174
	v_mul_f32_e32 v175, 0xbfb8aa3b, v175
	v_exp_f32_e32 v0, v0
	v_exp_f32_e32 v151, v151
	v_exp_f32_e32 v167, v167
	v_exp_f32_e32 v169, v169
	v_exp_f32_e32 v170, v170
	v_exp_f32_e32 v171, v171
	v_exp_f32_e32 v174, v174
	v_exp_f32_e32 v175, v175
	v_add_f32_e32 v0, 1.0, v0
	v_add_f32_e32 v151, 1.0, v151
	v_add_f32_e32 v167, 1.0, v167
	v_add_f32_e32 v169, 1.0, v169
	v_add_f32_e32 v170, 1.0, v170
	v_add_f32_e32 v171, 1.0, v171
	v_add_f32_e32 v174, 1.0, v174
	v_add_f32_e32 v175, 1.0, v175
	v_rcp_f32_e32 v0, v0
	v_rcp_f32_e32 v151, v151
	v_rcp_f32_e32 v167, v167
	v_rcp_f32_e32 v169, v169
	v_rcp_f32_e32 v170, v170
	v_rcp_f32_e32 v171, v171
	v_rcp_f32_e32 v174, v174
	v_rcp_f32_e32 v175, v175
	v_mul_f32_e32 v0, v46, v0
	v_mul_f32_e32 v151, v47, v151
	v_mul_f32_e32 v167, v48, v167
	v_mul_f32_e32 v169, v49, v169
	v_mul_f32_e32 v170, v42, v170
	v_mul_f32_e32 v171, v43, v171
	v_mul_f32_e32 v174, v44, v174
	v_mul_f32_e32 v175, v45, v175
	v_cvt_pk_bf16_f32 v46, v0, v151
	v_cvt_pk_bf16_f32 v47, v167, v169
	v_cvt_pk_bf16_f32 v48, v170, v171
	v_cvt_pk_bf16_f32 v49, v174, v175
	v_or_b32_e32 v172, 144, v150
	v_mov_b32_e32 v173, 0
	v_lshlrev_b64 v[172:173], 12, v[172:173]
	v_lshl_add_u64 v[172:173], s[6:7], 0, v[172:173]
	v_lshl_add_u64 v[172:173], v[172:173], 0, v[146:147]
	global_store_dwordx4 v[172:173], v[46:49], off
	s_waitcnt vmcnt(15)
	v_lshlrev_b32_e32 v0, 16, v220
	v_and_b32_e32 v151, 0xffff0000, v220
	v_lshlrev_b32_e32 v167, 16, v221
	v_and_b32_e32 v169, 0xffff0000, v221
	v_lshlrev_b32_e32 v170, 16, v222
	v_and_b32_e32 v171, 0xffff0000, v222
	v_lshlrev_b32_e32 v174, 16, v223
	v_and_b32_e32 v175, 0xffff0000, v223
	v_mul_f32_e32 v0, 0xbfb8aa3b, v0
	v_mul_f32_e32 v151, 0xbfb8aa3b, v151
	v_mul_f32_e32 v167, 0xbfb8aa3b, v167
	v_mul_f32_e32 v169, 0xbfb8aa3b, v169
	v_mul_f32_e32 v170, 0xbfb8aa3b, v170
	v_mul_f32_e32 v171, 0xbfb8aa3b, v171
	v_mul_f32_e32 v174, 0xbfb8aa3b, v174
	v_mul_f32_e32 v175, 0xbfb8aa3b, v175
	v_exp_f32_e32 v0, v0
	v_exp_f32_e32 v151, v151
	v_exp_f32_e32 v167, v167
	v_exp_f32_e32 v169, v169
	v_exp_f32_e32 v170, v170
	v_exp_f32_e32 v171, v171
	v_exp_f32_e32 v174, v174
	v_exp_f32_e32 v175, v175
	v_add_f32_e32 v0, 1.0, v0
	v_add_f32_e32 v151, 1.0, v151
	v_add_f32_e32 v167, 1.0, v167
	v_add_f32_e32 v169, 1.0, v169
	v_add_f32_e32 v170, 1.0, v170
	v_add_f32_e32 v171, 1.0, v171
	v_add_f32_e32 v174, 1.0, v174
	v_add_f32_e32 v175, 1.0, v175
	v_rcp_f32_e32 v0, v0
	v_rcp_f32_e32 v151, v151
	v_rcp_f32_e32 v167, v167
	v_rcp_f32_e32 v169, v169
	v_rcp_f32_e32 v170, v170
	v_rcp_f32_e32 v171, v171
	v_rcp_f32_e32 v174, v174
	v_rcp_f32_e32 v175, v175
	v_mul_f32_e32 v0, v38, v0
	v_mul_f32_e32 v151, v39, v151
	v_mul_f32_e32 v167, v40, v167
	v_mul_f32_e32 v169, v41, v169
	v_mul_f32_e32 v170, v34, v170
	v_mul_f32_e32 v171, v35, v171
	v_mul_f32_e32 v174, v36, v174
	v_mul_f32_e32 v175, v37, v175
	v_cvt_pk_bf16_f32 v38, v0, v151
	v_cvt_pk_bf16_f32 v39, v167, v169
	v_cvt_pk_bf16_f32 v40, v170, v171
	v_cvt_pk_bf16_f32 v41, v174, v175
	global_store_dwordx4 v[172:173], v[38:41], off offset:256
	s_waitcnt vmcnt(15)
	v_lshlrev_b32_e32 v0, 16, v224
	v_and_b32_e32 v151, 0xffff0000, v224
	v_lshlrev_b32_e32 v167, 16, v225
	v_and_b32_e32 v169, 0xffff0000, v225
	v_lshlrev_b32_e32 v170, 16, v226
	v_and_b32_e32 v171, 0xffff0000, v226
	v_lshlrev_b32_e32 v174, 16, v227
	v_and_b32_e32 v175, 0xffff0000, v227
	v_mul_f32_e32 v0, 0xbfb8aa3b, v0
	v_mul_f32_e32 v151, 0xbfb8aa3b, v151
	v_mul_f32_e32 v167, 0xbfb8aa3b, v167
	v_mul_f32_e32 v169, 0xbfb8aa3b, v169
	v_mul_f32_e32 v170, 0xbfb8aa3b, v170
	v_mul_f32_e32 v171, 0xbfb8aa3b, v171
	v_mul_f32_e32 v174, 0xbfb8aa3b, v174
	v_mul_f32_e32 v175, 0xbfb8aa3b, v175
	v_exp_f32_e32 v0, v0
	v_exp_f32_e32 v151, v151
	v_exp_f32_e32 v167, v167
	v_exp_f32_e32 v169, v169
	v_exp_f32_e32 v170, v170
	v_exp_f32_e32 v171, v171
	v_exp_f32_e32 v174, v174
	v_exp_f32_e32 v175, v175
	v_add_f32_e32 v0, 1.0, v0
	v_add_f32_e32 v151, 1.0, v151
	v_add_f32_e32 v167, 1.0, v167
	v_add_f32_e32 v169, 1.0, v169
	v_add_f32_e32 v170, 1.0, v170
	v_add_f32_e32 v171, 1.0, v171
	v_add_f32_e32 v174, 1.0, v174
	v_add_f32_e32 v175, 1.0, v175
	v_rcp_f32_e32 v0, v0
	v_rcp_f32_e32 v151, v151
	v_rcp_f32_e32 v167, v167
	v_rcp_f32_e32 v169, v169
	v_rcp_f32_e32 v170, v170
	v_rcp_f32_e32 v171, v171
	v_rcp_f32_e32 v174, v174
	v_rcp_f32_e32 v175, v175
	v_mul_f32_e32 v0, v30, v0
	v_mul_f32_e32 v151, v31, v151
	v_mul_f32_e32 v167, v32, v167
	v_mul_f32_e32 v169, v33, v169
	v_mul_f32_e32 v170, v26, v170
	v_mul_f32_e32 v171, v27, v171
	v_mul_f32_e32 v174, v28, v174
	v_mul_f32_e32 v175, v29, v175
	v_cvt_pk_bf16_f32 v30, v0, v151
	v_cvt_pk_bf16_f32 v31, v167, v169
	v_cvt_pk_bf16_f32 v32, v170, v171
	v_cvt_pk_bf16_f32 v33, v174, v175
	v_or_b32_e32 v172, 160, v150
	v_mov_b32_e32 v173, 0
	v_lshlrev_b64 v[172:173], 12, v[172:173]
	v_lshl_add_u64 v[172:173], s[6:7], 0, v[172:173]
	v_lshl_add_u64 v[172:173], v[172:173], 0, v[146:147]
	global_store_dwordx4 v[172:173], v[30:33], off
	s_waitcnt vmcnt(15)
	v_lshlrev_b32_e32 v0, 16, v228
	v_and_b32_e32 v151, 0xffff0000, v228
	v_lshlrev_b32_e32 v167, 16, v229
	v_and_b32_e32 v169, 0xffff0000, v229
	v_lshlrev_b32_e32 v170, 16, v230
	v_and_b32_e32 v171, 0xffff0000, v230
	v_lshlrev_b32_e32 v174, 16, v231
	v_and_b32_e32 v175, 0xffff0000, v231
	v_mul_f32_e32 v0, 0xbfb8aa3b, v0
	v_mul_f32_e32 v151, 0xbfb8aa3b, v151
	v_mul_f32_e32 v167, 0xbfb8aa3b, v167
	v_mul_f32_e32 v169, 0xbfb8aa3b, v169
	v_mul_f32_e32 v170, 0xbfb8aa3b, v170
	v_mul_f32_e32 v171, 0xbfb8aa3b, v171
	v_mul_f32_e32 v174, 0xbfb8aa3b, v174
	v_mul_f32_e32 v175, 0xbfb8aa3b, v175
	v_exp_f32_e32 v0, v0
	v_exp_f32_e32 v151, v151
	v_exp_f32_e32 v167, v167
	v_exp_f32_e32 v169, v169
	v_exp_f32_e32 v170, v170
	v_exp_f32_e32 v171, v171
	v_exp_f32_e32 v174, v174
	v_exp_f32_e32 v175, v175
	v_add_f32_e32 v0, 1.0, v0
	v_add_f32_e32 v151, 1.0, v151
	v_add_f32_e32 v167, 1.0, v167
	v_add_f32_e32 v169, 1.0, v169
	v_add_f32_e32 v170, 1.0, v170
	v_add_f32_e32 v171, 1.0, v171
	v_add_f32_e32 v174, 1.0, v174
	v_add_f32_e32 v175, 1.0, v175
	v_rcp_f32_e32 v0, v0
	v_rcp_f32_e32 v151, v151
	v_rcp_f32_e32 v167, v167
	v_rcp_f32_e32 v169, v169
	v_rcp_f32_e32 v170, v170
	v_rcp_f32_e32 v171, v171
	v_rcp_f32_e32 v174, v174
	v_rcp_f32_e32 v175, v175
	v_mul_f32_e32 v0, v22, v0
	v_mul_f32_e32 v151, v23, v151
	v_mul_f32_e32 v167, v24, v167
	v_mul_f32_e32 v169, v25, v169
	v_mul_f32_e32 v170, v18, v170
	v_mul_f32_e32 v171, v19, v171
	v_mul_f32_e32 v174, v20, v174
	v_mul_f32_e32 v175, v21, v175
	v_cvt_pk_bf16_f32 v22, v0, v151
	v_cvt_pk_bf16_f32 v23, v167, v169
	v_cvt_pk_bf16_f32 v24, v170, v171
	v_cvt_pk_bf16_f32 v25, v174, v175
	global_store_dwordx4 v[172:173], v[22:25], off offset:256
	s_waitcnt vmcnt(15)
	v_lshlrev_b32_e32 v0, 16, v232
	v_and_b32_e32 v151, 0xffff0000, v232
	v_lshlrev_b32_e32 v167, 16, v233
	v_and_b32_e32 v169, 0xffff0000, v233
	v_lshlrev_b32_e32 v170, 16, v234
	v_and_b32_e32 v171, 0xffff0000, v234
	v_lshlrev_b32_e32 v174, 16, v235
	v_and_b32_e32 v175, 0xffff0000, v235
	v_mul_f32_e32 v0, 0xbfb8aa3b, v0
	v_mul_f32_e32 v151, 0xbfb8aa3b, v151
	v_mul_f32_e32 v167, 0xbfb8aa3b, v167
	v_mul_f32_e32 v169, 0xbfb8aa3b, v169
	v_mul_f32_e32 v170, 0xbfb8aa3b, v170
	v_mul_f32_e32 v171, 0xbfb8aa3b, v171
	v_mul_f32_e32 v174, 0xbfb8aa3b, v174
	v_mul_f32_e32 v175, 0xbfb8aa3b, v175
	v_exp_f32_e32 v0, v0
	v_exp_f32_e32 v151, v151
	v_exp_f32_e32 v167, v167
	v_exp_f32_e32 v169, v169
	v_exp_f32_e32 v170, v170
	v_exp_f32_e32 v171, v171
	v_exp_f32_e32 v174, v174
	v_exp_f32_e32 v175, v175
	v_add_f32_e32 v0, 1.0, v0
	v_add_f32_e32 v151, 1.0, v151
	v_add_f32_e32 v167, 1.0, v167
	v_add_f32_e32 v169, 1.0, v169
	v_add_f32_e32 v170, 1.0, v170
	v_add_f32_e32 v171, 1.0, v171
	v_add_f32_e32 v174, 1.0, v174
	v_add_f32_e32 v175, 1.0, v175
	v_rcp_f32_e32 v0, v0
	v_rcp_f32_e32 v151, v151
	v_rcp_f32_e32 v167, v167
	v_rcp_f32_e32 v169, v169
	v_rcp_f32_e32 v170, v170
	v_rcp_f32_e32 v171, v171
	v_rcp_f32_e32 v174, v174
	v_rcp_f32_e32 v175, v175
	v_mul_f32_e32 v0, v14, v0
	v_mul_f32_e32 v151, v15, v151
	v_mul_f32_e32 v167, v16, v167
	v_mul_f32_e32 v169, v17, v169
	v_mul_f32_e32 v170, v10, v170
	v_mul_f32_e32 v171, v11, v171
	v_mul_f32_e32 v174, v12, v174
	v_mul_f32_e32 v175, v13, v175
	v_cvt_pk_bf16_f32 v14, v0, v151
	v_cvt_pk_bf16_f32 v15, v167, v169
	v_cvt_pk_bf16_f32 v16, v170, v171
	v_cvt_pk_bf16_f32 v17, v174, v175
	v_or_b32_e32 v172, 176, v150
	v_mov_b32_e32 v173, 0
	v_lshlrev_b64 v[172:173], 12, v[172:173]
	v_lshl_add_u64 v[172:173], s[6:7], 0, v[172:173]
	v_lshl_add_u64 v[172:173], v[172:173], 0, v[146:147]
	global_store_dwordx4 v[172:173], v[14:17], off
	s_waitcnt vmcnt(15)
	v_lshlrev_b32_e32 v0, 16, v236
	v_and_b32_e32 v151, 0xffff0000, v236
	v_lshlrev_b32_e32 v167, 16, v237
	v_and_b32_e32 v169, 0xffff0000, v237
	v_lshlrev_b32_e32 v170, 16, v238
	v_and_b32_e32 v171, 0xffff0000, v238
	v_lshlrev_b32_e32 v174, 16, v239
	v_and_b32_e32 v175, 0xffff0000, v239
	v_mul_f32_e32 v0, 0xbfb8aa3b, v0
	v_mul_f32_e32 v151, 0xbfb8aa3b, v151
	v_mul_f32_e32 v167, 0xbfb8aa3b, v167
	v_mul_f32_e32 v169, 0xbfb8aa3b, v169
	v_mul_f32_e32 v170, 0xbfb8aa3b, v170
	v_mul_f32_e32 v171, 0xbfb8aa3b, v171
	v_mul_f32_e32 v174, 0xbfb8aa3b, v174
	v_mul_f32_e32 v175, 0xbfb8aa3b, v175
	v_exp_f32_e32 v0, v0
	v_exp_f32_e32 v151, v151
	v_exp_f32_e32 v167, v167
	v_exp_f32_e32 v169, v169
	v_exp_f32_e32 v170, v170
	v_exp_f32_e32 v171, v171
	v_exp_f32_e32 v174, v174
	v_exp_f32_e32 v175, v175
	v_add_f32_e32 v0, 1.0, v0
	v_add_f32_e32 v151, 1.0, v151
	v_add_f32_e32 v167, 1.0, v167
	v_add_f32_e32 v169, 1.0, v169
	v_add_f32_e32 v170, 1.0, v170
	v_add_f32_e32 v171, 1.0, v171
	v_add_f32_e32 v174, 1.0, v174
	v_add_f32_e32 v175, 1.0, v175
	v_rcp_f32_e32 v0, v0
	v_rcp_f32_e32 v151, v151
	v_rcp_f32_e32 v167, v167
	v_rcp_f32_e32 v169, v169
	v_rcp_f32_e32 v170, v170
	v_rcp_f32_e32 v171, v171
	v_rcp_f32_e32 v174, v174
	v_rcp_f32_e32 v175, v175
	v_mul_f32_e32 v0, v6, v0
	v_mul_f32_e32 v151, v7, v151
	v_mul_f32_e32 v167, v8, v167
	v_mul_f32_e32 v169, v9, v169
	v_mul_f32_e32 v170, v2, v170
	v_mul_f32_e32 v171, v3, v171
	v_mul_f32_e32 v174, v4, v174
	v_mul_f32_e32 v175, v5, v175
	v_cvt_pk_bf16_f32 v6, v0, v151
	v_cvt_pk_bf16_f32 v7, v167, v169
	v_cvt_pk_bf16_f32 v8, v170, v171
	v_cvt_pk_bf16_f32 v9, v174, v175
	global_store_dwordx4 v[172:173], v[6:9], off offset:256
	s_andn2_b64 vcc, exec, s[4:5]
	s_mov_b64 s[4:5], -1
	s_cbranch_vccnz .LBB0_1121
	s_andn2_b64 vcc, exec, s[10:11]
	s_cbranch_vccnz .LBB0_1120
	s_barrier
	s_branch .LBB0_1120

.LBB0_1156:
	v_lshl_add_u32 v150, s26, 8, v158
	v_lshl_or_b32 v148, s51, 8, v157
	v_mov_b64_e32 v[152:153], s[96:97]
	v_ashrrev_i32_e32 v149, 31, v148
	v_lshlrev_b64 v[146:147], 1, v[148:149]
	v_or_b32_e32 v148, 0x80, v148
	v_ashrrev_i32_e32 v149, 31, v148
	v_lshlrev_b64 v[148:149], 1, v[148:149]
	v_mov_b32_e32 v168, v150
	v_mad_i64_i32 v[172:173], s[0:1], v168, s50, v[152:153]
	v_lshl_add_u64 v[172:173], v[172:173], 0, s[16:17]
	v_mov_b32_e32 v169, 0
	v_lshlrev_b64 v[174:175], 12, v[168:169]
	v_lshl_add_u64 v[174:175], s[6:7], 0, v[174:175]
	v_lshl_add_u64 v[174:175], v[174:175], 0, v[146:147]
	v_lshl_add_u64 v[178:179], v[172:173], 0, v[146:147]
	global_load_dwordx4 v[180:183], v[178:179], off nt
	global_load_dwordx4 v[184:187], v[174:175], off
	v_lshl_add_u64 v[178:179], v[172:173], 0, v[148:149]
	global_load_dwordx4 v[188:191], v[178:179], off nt
	global_load_dwordx4 v[192:195], v[174:175], off offset:256
	v_or_b32_e32 v168, 16, v150
	v_mad_i64_i32 v[172:173], s[0:1], v168, s50, v[152:153]
	v_lshl_add_u64 v[172:173], v[172:173], 0, s[16:17]
	v_mov_b32_e32 v169, 0
	v_lshlrev_b64 v[174:175], 12, v[168:169]
	v_lshl_add_u64 v[174:175], s[6:7], 0, v[174:175]
	v_lshl_add_u64 v[174:175], v[174:175], 0, v[146:147]
	v_lshl_add_u64 v[178:179], v[172:173], 0, v[146:147]
	global_load_dwordx4 v[196:199], v[178:179], off nt
	global_load_dwordx4 v[200:203], v[174:175], off
	v_lshl_add_u64 v[178:179], v[172:173], 0, v[148:149]
	global_load_dwordx4 v[204:207], v[178:179], off nt
	global_load_dwordx4 v[208:211], v[174:175], off offset:256
	v_or_b32_e32 v168, 32, v150
	v_mad_i64_i32 v[172:173], s[0:1], v168, s50, v[152:153]
	v_lshl_add_u64 v[172:173], v[172:173], 0, s[16:17]
	v_mov_b32_e32 v169, 0
	v_lshlrev_b64 v[174:175], 12, v[168:169]
	v_lshl_add_u64 v[174:175], s[6:7], 0, v[174:175]
	v_lshl_add_u64 v[174:175], v[174:175], 0, v[146:147]
	v_lshl_add_u64 v[178:179], v[172:173], 0, v[146:147]
	global_load_dwordx4 v[212:215], v[178:179], off nt
	global_load_dwordx4 v[222:225], v[174:175], off
	v_lshl_add_u64 v[178:179], v[172:173], 0, v[148:149]
	global_load_dwordx4 v[226:229], v[178:179], off nt
	global_load_dwordx4 v[230:233], v[174:175], off offset:256
	v_or_b32_e32 v168, 48, v150
	v_mad_i64_i32 v[172:173], s[0:1], v168, s50, v[152:153]
	v_lshl_add_u64 v[172:173], v[172:173], 0, s[16:17]
	v_mov_b32_e32 v169, 0
	v_lshlrev_b64 v[174:175], 12, v[168:169]
	v_lshl_add_u64 v[174:175], s[6:7], 0, v[174:175]
	v_lshl_add_u64 v[174:175], v[174:175], 0, v[146:147]
	v_lshl_add_u64 v[178:179], v[172:173], 0, v[146:147]
	global_load_dwordx4 v[234:237], v[178:179], off nt
	global_load_dwordx4 v[238:241], v[174:175], off
	v_lshl_add_u64 v[178:179], v[172:173], 0, v[148:149]
	global_load_dwordx4 v[242:245], v[178:179], off nt
	global_load_dwordx4 v[246:249], v[174:175], off offset:256
	s_waitcnt vmcnt(14)
	v_lshlrev_b32_e32 v0, 16, v180
	v_and_b32_e32 v151, 0xffff0000, v180
	v_lshlrev_b32_e32 v160, 16, v181
	v_and_b32_e32 v161, 0xffff0000, v181
	v_lshlrev_b32_e32 v162, 16, v182
	v_and_b32_e32 v163, 0xffff0000, v182
	v_lshlrev_b32_e32 v164, 16, v183
	v_and_b32_e32 v165, 0xffff0000, v183
	v_mul_f32_e32 v0, 0xbfb8aa3b, v0
	v_mul_f32_e32 v151, 0xbfb8aa3b, v151
	v_mul_f32_e32 v160, 0xbfb8aa3b, v160
	v_mul_f32_e32 v161, 0xbfb8aa3b, v161
	v_mul_f32_e32 v162, 0xbfb8aa3b, v162
	v_mul_f32_e32 v163, 0xbfb8aa3b, v163
	v_mul_f32_e32 v164, 0xbfb8aa3b, v164
	v_mul_f32_e32 v165, 0xbfb8aa3b, v165
	v_exp_f32_e32 v0, v0
	v_exp_f32_e32 v151, v151
	v_exp_f32_e32 v160, v160
	v_exp_f32_e32 v161, v161
	v_exp_f32_e32 v162, v162
	v_exp_f32_e32 v163, v163
	v_exp_f32_e32 v164, v164
	v_exp_f32_e32 v165, v165
	v_add_f32_e32 v0, 1.0, v0
	v_add_f32_e32 v151, 1.0, v151
	v_add_f32_e32 v160, 1.0, v160
	v_add_f32_e32 v161, 1.0, v161
	v_add_f32_e32 v162, 1.0, v162
	v_add_f32_e32 v163, 1.0, v163
	v_add_f32_e32 v164, 1.0, v164
	v_add_f32_e32 v165, 1.0, v165
	v_rcp_f32_e32 v0, v0
	v_rcp_f32_e32 v151, v151
	v_rcp_f32_e32 v160, v160
	v_rcp_f32_e32 v161, v161
	v_rcp_f32_e32 v162, v162
	v_rcp_f32_e32 v163, v163
	v_rcp_f32_e32 v164, v164
	v_rcp_f32_e32 v165, v165
	v_lshlrev_b32_e32 v166, 16, v184
	v_and_b32_e32 v184, 0xffff0000, v184
	v_lshlrev_b32_e32 v167, 16, v185
	v_and_b32_e32 v185, 0xffff0000, v185
	v_lshlrev_b32_e32 v170, 16, v186
	v_and_b32_e32 v186, 0xffff0000, v186
	v_lshlrev_b32_e32 v171, 16, v187
	v_and_b32_e32 v187, 0xffff0000, v187
	v_fmac_f32_e32 v166, v126, v0
	v_fmac_f32_e32 v184, v127, v151
	v_fmac_f32_e32 v167, v128, v160
	v_fmac_f32_e32 v185, v129, v161
	v_fmac_f32_e32 v170, v122, v162
	v_fmac_f32_e32 v186, v123, v163
	v_fmac_f32_e32 v171, v124, v164
	v_fmac_f32_e32 v187, v125, v165
	v_cvt_pk_bf16_f32 v184, v166, v184
	v_cvt_pk_bf16_f32 v185, v167, v185
	v_cvt_pk_bf16_f32 v186, v170, v186
	v_cvt_pk_bf16_f32 v187, v171, v187
	v_mov_b32_e32 v176, v150
	v_mov_b32_e32 v177, 0
	v_lshlrev_b64 v[176:177], 12, v[176:177]
	v_lshl_add_u64 v[176:177], s[10:11], 0, v[176:177]
	v_lshl_add_u64 v[176:177], v[176:177], 0, v[146:147]
	global_store_dwordx4 v[176:177], v[184:187], off
	v_or_b32_e32 v168, 128, v150
	v_mad_i64_i32 v[172:173], s[0:1], v168, s50, v[152:153]
	v_lshl_add_u64 v[172:173], v[172:173], 0, s[16:17]
	v_mov_b32_e32 v169, 0
	v_lshlrev_b64 v[174:175], 12, v[168:169]
	v_lshl_add_u64 v[174:175], s[6:7], 0, v[174:175]
	v_lshl_add_u64 v[174:175], v[174:175], 0, v[146:147]
	v_lshl_add_u64 v[178:179], v[172:173], 0, v[146:147]
	global_load_dwordx4 v[122:125], v[178:179], off nt
	global_load_dwordx4 v[126:129], v[174:175], off
	s_waitcnt vmcnt(15)
	v_lshlrev_b32_e32 v0, 16, v188
	v_and_b32_e32 v151, 0xffff0000, v188
	v_lshlrev_b32_e32 v160, 16, v189
	v_and_b32_e32 v161, 0xffff0000, v189
	v_lshlrev_b32_e32 v162, 16, v190
	v_and_b32_e32 v163, 0xffff0000, v190
	v_lshlrev_b32_e32 v164, 16, v191
	v_and_b32_e32 v165, 0xffff0000, v191
	v_mul_f32_e32 v0, 0xbfb8aa3b, v0
	v_mul_f32_e32 v151, 0xbfb8aa3b, v151
	v_mul_f32_e32 v160, 0xbfb8aa3b, v160
	v_mul_f32_e32 v161, 0xbfb8aa3b, v161
	v_mul_f32_e32 v162, 0xbfb8aa3b, v162
	v_mul_f32_e32 v163, 0xbfb8aa3b, v163
	v_mul_f32_e32 v164, 0xbfb8aa3b, v164
	v_mul_f32_e32 v165, 0xbfb8aa3b, v165
	v_exp_f32_e32 v0, v0
	v_exp_f32_e32 v151, v151
	v_exp_f32_e32 v160, v160
	v_exp_f32_e32 v161, v161
	v_exp_f32_e32 v162, v162
	v_exp_f32_e32 v163, v163
	v_exp_f32_e32 v164, v164
	v_exp_f32_e32 v165, v165
	v_add_f32_e32 v0, 1.0, v0
	v_add_f32_e32 v151, 1.0, v151
	v_add_f32_e32 v160, 1.0, v160
	v_add_f32_e32 v161, 1.0, v161
	v_add_f32_e32 v162, 1.0, v162
	v_add_f32_e32 v163, 1.0, v163
	v_add_f32_e32 v164, 1.0, v164
	v_add_f32_e32 v165, 1.0, v165
	v_rcp_f32_e32 v0, v0
	v_rcp_f32_e32 v151, v151
	v_rcp_f32_e32 v160, v160
	v_rcp_f32_e32 v161, v161
	v_rcp_f32_e32 v162, v162
	v_rcp_f32_e32 v163, v163
	v_rcp_f32_e32 v164, v164
	v_rcp_f32_e32 v165, v165
	v_lshlrev_b32_e32 v166, 16, v192
	v_and_b32_e32 v192, 0xffff0000, v192
	v_lshlrev_b32_e32 v167, 16, v193
	v_and_b32_e32 v193, 0xffff0000, v193
	v_lshlrev_b32_e32 v170, 16, v194
	v_and_b32_e32 v194, 0xffff0000, v194
	v_lshlrev_b32_e32 v171, 16, v195
	v_and_b32_e32 v195, 0xffff0000, v195
	v_fmac_f32_e32 v166, v118, v0
	v_fmac_f32_e32 v192, v119, v151
	v_fmac_f32_e32 v167, v120, v160
	v_fmac_f32_e32 v193, v121, v161
	v_fmac_f32_e32 v170, v114, v162
	v_fmac_f32_e32 v194, v115, v163
	v_fmac_f32_e32 v171, v116, v164
	v_fmac_f32_e32 v195, v117, v165
	v_cvt_pk_bf16_f32 v192, v166, v192
	v_cvt_pk_bf16_f32 v193, v167, v193
	v_cvt_pk_bf16_f32 v194, v170, v194
	v_cvt_pk_bf16_f32 v195, v171, v195
	global_store_dwordx4 v[176:177], v[192:195], off offset:256
	v_lshl_add_u64 v[178:179], v[172:173], 0, v[148:149]
	global_load_dwordx4 v[114:117], v[178:179], off nt
	global_load_dwordx4 v[118:121], v[174:175], off offset:256
	s_waitcnt vmcnt(16)
	v_lshlrev_b32_e32 v0, 16, v196
	v_and_b32_e32 v151, 0xffff0000, v196
	v_lshlrev_b32_e32 v160, 16, v197
	v_and_b32_e32 v161, 0xffff0000, v197
	v_lshlrev_b32_e32 v162, 16, v198
	v_and_b32_e32 v163, 0xffff0000, v198
	v_lshlrev_b32_e32 v164, 16, v199
	v_and_b32_e32 v165, 0xffff0000, v199
	v_mul_f32_e32 v0, 0xbfb8aa3b, v0
	v_mul_f32_e32 v151, 0xbfb8aa3b, v151
	v_mul_f32_e32 v160, 0xbfb8aa3b, v160
	v_mul_f32_e32 v161, 0xbfb8aa3b, v161
	v_mul_f32_e32 v162, 0xbfb8aa3b, v162
	v_mul_f32_e32 v163, 0xbfb8aa3b, v163
	v_mul_f32_e32 v164, 0xbfb8aa3b, v164
	v_mul_f32_e32 v165, 0xbfb8aa3b, v165
	v_exp_f32_e32 v0, v0
	v_exp_f32_e32 v151, v151
	v_exp_f32_e32 v160, v160
	v_exp_f32_e32 v161, v161
	v_exp_f32_e32 v162, v162
	v_exp_f32_e32 v163, v163
	v_exp_f32_e32 v164, v164
	v_exp_f32_e32 v165, v165
	v_add_f32_e32 v0, 1.0, v0
	v_add_f32_e32 v151, 1.0, v151
	v_add_f32_e32 v160, 1.0, v160
	v_add_f32_e32 v161, 1.0, v161
	v_add_f32_e32 v162, 1.0, v162
	v_add_f32_e32 v163, 1.0, v163
	v_add_f32_e32 v164, 1.0, v164
	v_add_f32_e32 v165, 1.0, v165
	v_rcp_f32_e32 v0, v0
	v_rcp_f32_e32 v151, v151
	v_rcp_f32_e32 v160, v160
	v_rcp_f32_e32 v161, v161
	v_rcp_f32_e32 v162, v162
	v_rcp_f32_e32 v163, v163
	v_rcp_f32_e32 v164, v164
	v_rcp_f32_e32 v165, v165
	v_lshlrev_b32_e32 v166, 16, v200
	v_and_b32_e32 v200, 0xffff0000, v200
	v_lshlrev_b32_e32 v167, 16, v201
	v_and_b32_e32 v201, 0xffff0000, v201
	v_lshlrev_b32_e32 v170, 16, v202
	v_and_b32_e32 v202, 0xffff0000, v202
	v_lshlrev_b32_e32 v171, 16, v203
	v_and_b32_e32 v203, 0xffff0000, v203
	v_fmac_f32_e32 v166, v110, v0
	v_fmac_f32_e32 v200, v111, v151
	v_fmac_f32_e32 v167, v112, v160
	v_fmac_f32_e32 v201, v113, v161
	v_fmac_f32_e32 v170, v106, v162
	v_fmac_f32_e32 v202, v107, v163
	v_fmac_f32_e32 v171, v108, v164
	v_fmac_f32_e32 v203, v109, v165
	v_cvt_pk_bf16_f32 v200, v166, v200
	v_cvt_pk_bf16_f32 v201, v167, v201
	v_cvt_pk_bf16_f32 v202, v170, v202
	v_cvt_pk_bf16_f32 v203, v171, v203
	v_or_b32_e32 v176, 16, v150
	v_mov_b32_e32 v177, 0
	v_lshlrev_b64 v[176:177], 12, v[176:177]
	v_lshl_add_u64 v[176:177], s[10:11], 0, v[176:177]
	v_lshl_add_u64 v[176:177], v[176:177], 0, v[146:147]
	global_store_dwordx4 v[176:177], v[200:203], off
	v_or_b32_e32 v168, 144, v150
	v_mad_i64_i32 v[172:173], s[0:1], v168, s50, v[152:153]
	v_lshl_add_u64 v[172:173], v[172:173], 0, s[16:17]
	v_mov_b32_e32 v169, 0
	v_lshlrev_b64 v[174:175], 12, v[168:169]
	v_lshl_add_u64 v[174:175], s[6:7], 0, v[174:175]
	v_lshl_add_u64 v[174:175], v[174:175], 0, v[146:147]
	v_lshl_add_u64 v[178:179], v[172:173], 0, v[146:147]
	global_load_dwordx4 v[106:109], v[178:179], off nt
	global_load_dwordx4 v[110:113], v[174:175], off
	s_waitcnt vmcnt(17)
	v_lshlrev_b32_e32 v0, 16, v204
	v_and_b32_e32 v151, 0xffff0000, v204
	v_lshlrev_b32_e32 v160, 16, v205
	v_and_b32_e32 v161, 0xffff0000, v205
	v_lshlrev_b32_e32 v162, 16, v206
	v_and_b32_e32 v163, 0xffff0000, v206
	v_lshlrev_b32_e32 v164, 16, v207
	v_and_b32_e32 v165, 0xffff0000, v207
	v_mul_f32_e32 v0, 0xbfb8aa3b, v0
	v_mul_f32_e32 v151, 0xbfb8aa3b, v151
	v_mul_f32_e32 v160, 0xbfb8aa3b, v160
	v_mul_f32_e32 v161, 0xbfb8aa3b, v161
	v_mul_f32_e32 v162, 0xbfb8aa3b, v162
	v_mul_f32_e32 v163, 0xbfb8aa3b, v163
	v_mul_f32_e32 v164, 0xbfb8aa3b, v164
	v_mul_f32_e32 v165, 0xbfb8aa3b, v165
	v_exp_f32_e32 v0, v0
	v_exp_f32_e32 v151, v151
	v_exp_f32_e32 v160, v160
	v_exp_f32_e32 v161, v161
	v_exp_f32_e32 v162, v162
	v_exp_f32_e32 v163, v163
	v_exp_f32_e32 v164, v164
	v_exp_f32_e32 v165, v165
	v_add_f32_e32 v0, 1.0, v0
	v_add_f32_e32 v151, 1.0, v151
	v_add_f32_e32 v160, 1.0, v160
	v_add_f32_e32 v161, 1.0, v161
	v_add_f32_e32 v162, 1.0, v162
	v_add_f32_e32 v163, 1.0, v163
	v_add_f32_e32 v164, 1.0, v164
	v_add_f32_e32 v165, 1.0, v165
	v_rcp_f32_e32 v0, v0
	v_rcp_f32_e32 v151, v151
	v_rcp_f32_e32 v160, v160
	v_rcp_f32_e32 v161, v161
	v_rcp_f32_e32 v162, v162
	v_rcp_f32_e32 v163, v163
	v_rcp_f32_e32 v164, v164
	v_rcp_f32_e32 v165, v165
	v_lshlrev_b32_e32 v166, 16, v208
	v_and_b32_e32 v208, 0xffff0000, v208
	v_lshlrev_b32_e32 v167, 16, v209
	v_and_b32_e32 v209, 0xffff0000, v209
	v_lshlrev_b32_e32 v170, 16, v210
	v_and_b32_e32 v210, 0xffff0000, v210
	v_lshlrev_b32_e32 v171, 16, v211
	v_and_b32_e32 v211, 0xffff0000, v211
	v_fmac_f32_e32 v166, v102, v0
	v_fmac_f32_e32 v208, v103, v151
	v_fmac_f32_e32 v167, v104, v160
	v_fmac_f32_e32 v209, v105, v161
	v_fmac_f32_e32 v170, v98, v162
	v_fmac_f32_e32 v210, v99, v163
	v_fmac_f32_e32 v171, v100, v164
	v_fmac_f32_e32 v211, v101, v165
	v_cvt_pk_bf16_f32 v208, v166, v208
	v_cvt_pk_bf16_f32 v209, v167, v209
	v_cvt_pk_bf16_f32 v210, v170, v210
	v_cvt_pk_bf16_f32 v211, v171, v211
	global_store_dwordx4 v[176:177], v[208:211], off offset:256
	v_lshl_add_u64 v[178:179], v[172:173], 0, v[148:149]
	global_load_dwordx4 v[98:101], v[178:179], off nt
	global_load_dwordx4 v[102:105], v[174:175], off offset:256
	s_waitcnt vmcnt(18)
	v_lshlrev_b32_e32 v0, 16, v212
	v_and_b32_e32 v151, 0xffff0000, v212
	v_lshlrev_b32_e32 v160, 16, v213
	v_and_b32_e32 v161, 0xffff0000, v213
	v_lshlrev_b32_e32 v162, 16, v214
	v_and_b32_e32 v163, 0xffff0000, v214
	v_lshlrev_b32_e32 v164, 16, v215
	v_and_b32_e32 v165, 0xffff0000, v215
	v_mul_f32_e32 v0, 0xbfb8aa3b, v0
	v_mul_f32_e32 v151, 0xbfb8aa3b, v151
	v_mul_f32_e32 v160, 0xbfb8aa3b, v160
	v_mul_f32_e32 v161, 0xbfb8aa3b, v161
	v_mul_f32_e32 v162, 0xbfb8aa3b, v162
	v_mul_f32_e32 v163, 0xbfb8aa3b, v163
	v_mul_f32_e32 v164, 0xbfb8aa3b, v164
	v_mul_f32_e32 v165, 0xbfb8aa3b, v165
	v_exp_f32_e32 v0, v0
	v_exp_f32_e32 v151, v151
	v_exp_f32_e32 v160, v160
	v_exp_f32_e32 v161, v161
	v_exp_f32_e32 v162, v162
	v_exp_f32_e32 v163, v163
	v_exp_f32_e32 v164, v164
	v_exp_f32_e32 v165, v165
	v_add_f32_e32 v0, 1.0, v0
	v_add_f32_e32 v151, 1.0, v151
	v_add_f32_e32 v160, 1.0, v160
	v_add_f32_e32 v161, 1.0, v161
	v_add_f32_e32 v162, 1.0, v162
	v_add_f32_e32 v163, 1.0, v163
	v_add_f32_e32 v164, 1.0, v164
	v_add_f32_e32 v165, 1.0, v165
	v_rcp_f32_e32 v0, v0
	v_rcp_f32_e32 v151, v151
	v_rcp_f32_e32 v160, v160
	v_rcp_f32_e32 v161, v161
	v_rcp_f32_e32 v162, v162
	v_rcp_f32_e32 v163, v163
	v_rcp_f32_e32 v164, v164
	v_rcp_f32_e32 v165, v165
	v_lshlrev_b32_e32 v166, 16, v222
	v_and_b32_e32 v222, 0xffff0000, v222
	v_lshlrev_b32_e32 v167, 16, v223
	v_and_b32_e32 v223, 0xffff0000, v223
	v_lshlrev_b32_e32 v170, 16, v224
	v_and_b32_e32 v224, 0xffff0000, v224
	v_lshlrev_b32_e32 v171, 16, v225
	v_and_b32_e32 v225, 0xffff0000, v225
	v_fmac_f32_e32 v166, v94, v0
	v_fmac_f32_e32 v222, v95, v151
	v_fmac_f32_e32 v167, v96, v160
	v_fmac_f32_e32 v223, v97, v161
	v_fmac_f32_e32 v170, v90, v162
	v_fmac_f32_e32 v224, v91, v163
	v_fmac_f32_e32 v171, v92, v164
	v_fmac_f32_e32 v225, v93, v165
	v_cvt_pk_bf16_f32 v222, v166, v222
	v_cvt_pk_bf16_f32 v223, v167, v223
	v_cvt_pk_bf16_f32 v224, v170, v224
	v_cvt_pk_bf16_f32 v225, v171, v225
	v_or_b32_e32 v176, 32, v150
	v_mov_b32_e32 v177, 0
	v_lshlrev_b64 v[176:177], 12, v[176:177]
	v_lshl_add_u64 v[176:177], s[10:11], 0, v[176:177]
	v_lshl_add_u64 v[176:177], v[176:177], 0, v[146:147]
	global_store_dwordx4 v[176:177], v[222:225], off
	v_or_b32_e32 v168, 160, v150
	v_mad_i64_i32 v[172:173], s[0:1], v168, s50, v[152:153]
	v_lshl_add_u64 v[172:173], v[172:173], 0, s[16:17]
	v_mov_b32_e32 v169, 0
	v_lshlrev_b64 v[174:175], 12, v[168:169]
	v_lshl_add_u64 v[174:175], s[6:7], 0, v[174:175]
	v_lshl_add_u64 v[174:175], v[174:175], 0, v[146:147]
	v_lshl_add_u64 v[178:179], v[172:173], 0, v[146:147]
	global_load_dwordx4 v[90:93], v[178:179], off nt
	global_load_dwordx4 v[94:97], v[174:175], off
	s_waitcnt vmcnt(19)
	v_lshlrev_b32_e32 v0, 16, v226
	v_and_b32_e32 v151, 0xffff0000, v226
	v_lshlrev_b32_e32 v160, 16, v227
	v_and_b32_e32 v161, 0xffff0000, v227
	v_lshlrev_b32_e32 v162, 16, v228
	v_and_b32_e32 v163, 0xffff0000, v228
	v_lshlrev_b32_e32 v164, 16, v229
	v_and_b32_e32 v165, 0xffff0000, v229
	v_mul_f32_e32 v0, 0xbfb8aa3b, v0
	v_mul_f32_e32 v151, 0xbfb8aa3b, v151
	v_mul_f32_e32 v160, 0xbfb8aa3b, v160
	v_mul_f32_e32 v161, 0xbfb8aa3b, v161
	v_mul_f32_e32 v162, 0xbfb8aa3b, v162
	v_mul_f32_e32 v163, 0xbfb8aa3b, v163
	v_mul_f32_e32 v164, 0xbfb8aa3b, v164
	v_mul_f32_e32 v165, 0xbfb8aa3b, v165
	v_exp_f32_e32 v0, v0
	v_exp_f32_e32 v151, v151
	v_exp_f32_e32 v160, v160
	v_exp_f32_e32 v161, v161
	v_exp_f32_e32 v162, v162
	v_exp_f32_e32 v163, v163
	v_exp_f32_e32 v164, v164
	v_exp_f32_e32 v165, v165
	v_add_f32_e32 v0, 1.0, v0
	v_add_f32_e32 v151, 1.0, v151
	v_add_f32_e32 v160, 1.0, v160
	v_add_f32_e32 v161, 1.0, v161
	v_add_f32_e32 v162, 1.0, v162
	v_add_f32_e32 v163, 1.0, v163
	v_add_f32_e32 v164, 1.0, v164
	v_add_f32_e32 v165, 1.0, v165
	v_rcp_f32_e32 v0, v0
	v_rcp_f32_e32 v151, v151
	v_rcp_f32_e32 v160, v160
	v_rcp_f32_e32 v161, v161
	v_rcp_f32_e32 v162, v162
	v_rcp_f32_e32 v163, v163
	v_rcp_f32_e32 v164, v164
	v_rcp_f32_e32 v165, v165
	v_lshlrev_b32_e32 v166, 16, v230
	v_and_b32_e32 v230, 0xffff0000, v230
	v_lshlrev_b32_e32 v167, 16, v231
	v_and_b32_e32 v231, 0xffff0000, v231
	v_lshlrev_b32_e32 v170, 16, v232
	v_and_b32_e32 v232, 0xffff0000, v232
	v_lshlrev_b32_e32 v171, 16, v233
	v_and_b32_e32 v233, 0xffff0000, v233
	v_fmac_f32_e32 v166, v86, v0
	v_fmac_f32_e32 v230, v87, v151
	v_fmac_f32_e32 v167, v88, v160
	v_fmac_f32_e32 v231, v89, v161
	v_fmac_f32_e32 v170, v82, v162
	v_fmac_f32_e32 v232, v83, v163
	v_fmac_f32_e32 v171, v84, v164
	v_fmac_f32_e32 v233, v85, v165
	v_cvt_pk_bf16_f32 v230, v166, v230
	v_cvt_pk_bf16_f32 v231, v167, v231
	v_cvt_pk_bf16_f32 v232, v170, v232
	v_cvt_pk_bf16_f32 v233, v171, v233
	global_store_dwordx4 v[176:177], v[230:233], off offset:256
	v_lshl_add_u64 v[178:179], v[172:173], 0, v[148:149]
	global_load_dwordx4 v[82:85], v[178:179], off nt
	global_load_dwordx4 v[86:89], v[174:175], off offset:256
	s_waitcnt vmcnt(20)
	v_lshlrev_b32_e32 v0, 16, v234
	v_and_b32_e32 v151, 0xffff0000, v234
	v_lshlrev_b32_e32 v160, 16, v235
	v_and_b32_e32 v161, 0xffff0000, v235
	v_lshlrev_b32_e32 v162, 16, v236
	v_and_b32_e32 v163, 0xffff0000, v236
	v_lshlrev_b32_e32 v164, 16, v237
	v_and_b32_e32 v165, 0xffff0000, v237
	v_mul_f32_e32 v0, 0xbfb8aa3b, v0
	v_mul_f32_e32 v151, 0xbfb8aa3b, v151
	v_mul_f32_e32 v160, 0xbfb8aa3b, v160
	v_mul_f32_e32 v161, 0xbfb8aa3b, v161
	v_mul_f32_e32 v162, 0xbfb8aa3b, v162
	v_mul_f32_e32 v163, 0xbfb8aa3b, v163
	v_mul_f32_e32 v164, 0xbfb8aa3b, v164
	v_mul_f32_e32 v165, 0xbfb8aa3b, v165
	v_exp_f32_e32 v0, v0
	v_exp_f32_e32 v151, v151
	v_exp_f32_e32 v160, v160
	v_exp_f32_e32 v161, v161
	v_exp_f32_e32 v162, v162
	v_exp_f32_e32 v163, v163
	v_exp_f32_e32 v164, v164
	v_exp_f32_e32 v165, v165
	v_add_f32_e32 v0, 1.0, v0
	v_add_f32_e32 v151, 1.0, v151
	v_add_f32_e32 v160, 1.0, v160
	v_add_f32_e32 v161, 1.0, v161
	v_add_f32_e32 v162, 1.0, v162
	v_add_f32_e32 v163, 1.0, v163
	v_add_f32_e32 v164, 1.0, v164
	v_add_f32_e32 v165, 1.0, v165
	v_rcp_f32_e32 v0, v0
	v_rcp_f32_e32 v151, v151
	v_rcp_f32_e32 v160, v160
	v_rcp_f32_e32 v161, v161
	v_rcp_f32_e32 v162, v162
	v_rcp_f32_e32 v163, v163
	v_rcp_f32_e32 v164, v164
	v_rcp_f32_e32 v165, v165
	v_lshlrev_b32_e32 v166, 16, v238
	v_and_b32_e32 v238, 0xffff0000, v238
	v_lshlrev_b32_e32 v167, 16, v239
	v_and_b32_e32 v239, 0xffff0000, v239
	v_lshlrev_b32_e32 v170, 16, v240
	v_and_b32_e32 v240, 0xffff0000, v240
	v_lshlrev_b32_e32 v171, 16, v241
	v_and_b32_e32 v241, 0xffff0000, v241
	v_fmac_f32_e32 v166, v78, v0
	v_fmac_f32_e32 v238, v79, v151
	v_fmac_f32_e32 v167, v80, v160
	v_fmac_f32_e32 v239, v81, v161
	v_fmac_f32_e32 v170, v74, v162
	v_fmac_f32_e32 v240, v75, v163
	v_fmac_f32_e32 v171, v76, v164
	v_fmac_f32_e32 v241, v77, v165
	v_cvt_pk_bf16_f32 v238, v166, v238
	v_cvt_pk_bf16_f32 v239, v167, v239
	v_cvt_pk_bf16_f32 v240, v170, v240
	v_cvt_pk_bf16_f32 v241, v171, v241
	v_or_b32_e32 v176, 48, v150
	v_mov_b32_e32 v177, 0
	v_lshlrev_b64 v[176:177], 12, v[176:177]
	v_lshl_add_u64 v[176:177], s[10:11], 0, v[176:177]
	v_lshl_add_u64 v[176:177], v[176:177], 0, v[146:147]
	global_store_dwordx4 v[176:177], v[238:241], off
	v_or_b32_e32 v168, 176, v150
	v_mad_i64_i32 v[172:173], s[0:1], v168, s50, v[152:153]
	v_lshl_add_u64 v[172:173], v[172:173], 0, s[16:17]
	v_mov_b32_e32 v169, 0
	v_lshlrev_b64 v[174:175], 12, v[168:169]
	v_lshl_add_u64 v[174:175], s[6:7], 0, v[174:175]
	v_lshl_add_u64 v[174:175], v[174:175], 0, v[146:147]
	v_lshl_add_u64 v[178:179], v[172:173], 0, v[146:147]
	global_load_dwordx4 v[74:77], v[178:179], off nt
	global_load_dwordx4 v[78:81], v[174:175], off
	s_waitcnt vmcnt(21)
	v_lshlrev_b32_e32 v0, 16, v242
	v_and_b32_e32 v151, 0xffff0000, v242
	v_lshlrev_b32_e32 v160, 16, v243
	v_and_b32_e32 v161, 0xffff0000, v243
	v_lshlrev_b32_e32 v162, 16, v244
	v_and_b32_e32 v163, 0xffff0000, v244
	v_lshlrev_b32_e32 v164, 16, v245
	v_and_b32_e32 v165, 0xffff0000, v245
	v_mul_f32_e32 v0, 0xbfb8aa3b, v0
	v_mul_f32_e32 v151, 0xbfb8aa3b, v151
	v_mul_f32_e32 v160, 0xbfb8aa3b, v160
	v_mul_f32_e32 v161, 0xbfb8aa3b, v161
	v_mul_f32_e32 v162, 0xbfb8aa3b, v162
	v_mul_f32_e32 v163, 0xbfb8aa3b, v163
	v_mul_f32_e32 v164, 0xbfb8aa3b, v164
	v_mul_f32_e32 v165, 0xbfb8aa3b, v165
	v_exp_f32_e32 v0, v0
	v_exp_f32_e32 v151, v151
	v_exp_f32_e32 v160, v160
	v_exp_f32_e32 v161, v161
	v_exp_f32_e32 v162, v162
	v_exp_f32_e32 v163, v163
	v_exp_f32_e32 v164, v164
	v_exp_f32_e32 v165, v165
	v_add_f32_e32 v0, 1.0, v0
	v_add_f32_e32 v151, 1.0, v151
	v_add_f32_e32 v160, 1.0, v160
	v_add_f32_e32 v161, 1.0, v161
	v_add_f32_e32 v162, 1.0, v162
	v_add_f32_e32 v163, 1.0, v163
	v_add_f32_e32 v164, 1.0, v164
	v_add_f32_e32 v165, 1.0, v165
	v_rcp_f32_e32 v0, v0
	v_rcp_f32_e32 v151, v151
	v_rcp_f32_e32 v160, v160
	v_rcp_f32_e32 v161, v161
	v_rcp_f32_e32 v162, v162
	v_rcp_f32_e32 v163, v163
	v_rcp_f32_e32 v164, v164
	v_rcp_f32_e32 v165, v165
	v_lshlrev_b32_e32 v166, 16, v246
	v_and_b32_e32 v246, 0xffff0000, v246
	v_lshlrev_b32_e32 v167, 16, v247
	v_and_b32_e32 v247, 0xffff0000, v247
	v_lshlrev_b32_e32 v170, 16, v248
	v_and_b32_e32 v248, 0xffff0000, v248
	v_lshlrev_b32_e32 v171, 16, v249
	v_and_b32_e32 v249, 0xffff0000, v249
	v_fmac_f32_e32 v166, v70, v0
	v_fmac_f32_e32 v246, v71, v151
	v_fmac_f32_e32 v167, v72, v160
	v_fmac_f32_e32 v247, v73, v161
	v_fmac_f32_e32 v170, v66, v162
	v_fmac_f32_e32 v248, v67, v163
	v_fmac_f32_e32 v171, v68, v164
	v_fmac_f32_e32 v249, v69, v165
	v_cvt_pk_bf16_f32 v246, v166, v246
	v_cvt_pk_bf16_f32 v247, v167, v247
	v_cvt_pk_bf16_f32 v248, v170, v248
	v_cvt_pk_bf16_f32 v249, v171, v249
	global_store_dwordx4 v[176:177], v[246:249], off offset:256
	v_lshl_add_u64 v[178:179], v[172:173], 0, v[148:149]
	global_load_dwordx4 v[66:69], v[178:179], off nt
	global_load_dwordx4 v[70:73], v[174:175], off offset:256
	s_waitcnt vmcnt(21)
	v_lshlrev_b32_e32 v0, 16, v122
	v_and_b32_e32 v151, 0xffff0000, v122
	v_lshlrev_b32_e32 v160, 16, v123
	v_and_b32_e32 v161, 0xffff0000, v123
	v_lshlrev_b32_e32 v162, 16, v124
	v_and_b32_e32 v163, 0xffff0000, v124
	v_lshlrev_b32_e32 v164, 16, v125
	v_and_b32_e32 v165, 0xffff0000, v125
	v_mul_f32_e32 v0, 0xbfb8aa3b, v0
	v_mul_f32_e32 v151, 0xbfb8aa3b, v151
	v_mul_f32_e32 v160, 0xbfb8aa3b, v160
	v_mul_f32_e32 v161, 0xbfb8aa3b, v161
	v_mul_f32_e32 v162, 0xbfb8aa3b, v162
	v_mul_f32_e32 v163, 0xbfb8aa3b, v163
	v_mul_f32_e32 v164, 0xbfb8aa3b, v164
	v_mul_f32_e32 v165, 0xbfb8aa3b, v165
	v_exp_f32_e32 v0, v0
	v_exp_f32_e32 v151, v151
	v_exp_f32_e32 v160, v160
	v_exp_f32_e32 v161, v161
	v_exp_f32_e32 v162, v162
	v_exp_f32_e32 v163, v163
	v_exp_f32_e32 v164, v164
	v_exp_f32_e32 v165, v165
	v_add_f32_e32 v0, 1.0, v0
	v_add_f32_e32 v151, 1.0, v151
	v_add_f32_e32 v160, 1.0, v160
	v_add_f32_e32 v161, 1.0, v161
	v_add_f32_e32 v162, 1.0, v162
	v_add_f32_e32 v163, 1.0, v163
	v_add_f32_e32 v164, 1.0, v164
	v_add_f32_e32 v165, 1.0, v165
	v_rcp_f32_e32 v0, v0
	v_rcp_f32_e32 v151, v151
	v_rcp_f32_e32 v160, v160
	v_rcp_f32_e32 v161, v161
	v_rcp_f32_e32 v162, v162
	v_rcp_f32_e32 v163, v163
	v_rcp_f32_e32 v164, v164
	v_rcp_f32_e32 v165, v165
	v_lshlrev_b32_e32 v166, 16, v126
	v_and_b32_e32 v126, 0xffff0000, v126
	v_lshlrev_b32_e32 v167, 16, v127
	v_and_b32_e32 v127, 0xffff0000, v127
	v_lshlrev_b32_e32 v170, 16, v128
	v_and_b32_e32 v128, 0xffff0000, v128
	v_lshlrev_b32_e32 v171, 16, v129
	v_and_b32_e32 v129, 0xffff0000, v129
	v_fmac_f32_e32 v166, v62, v0
	v_fmac_f32_e32 v126, v63, v151
	v_fmac_f32_e32 v167, v64, v160
	v_fmac_f32_e32 v127, v65, v161
	v_fmac_f32_e32 v170, v58, v162
	v_fmac_f32_e32 v128, v59, v163
	v_fmac_f32_e32 v171, v60, v164
	v_fmac_f32_e32 v129, v61, v165
	v_cvt_pk_bf16_f32 v126, v166, v126
	v_cvt_pk_bf16_f32 v127, v167, v127
	v_cvt_pk_bf16_f32 v128, v170, v128
	v_cvt_pk_bf16_f32 v129, v171, v129
	v_or_b32_e32 v176, 128, v150
	v_mov_b32_e32 v177, 0
	v_lshlrev_b64 v[176:177], 12, v[176:177]
	v_lshl_add_u64 v[176:177], s[10:11], 0, v[176:177]
	v_lshl_add_u64 v[176:177], v[176:177], 0, v[146:147]
	global_store_dwordx4 v[176:177], v[126:129], off
	s_waitcnt vmcnt(19)
	v_lshlrev_b32_e32 v0, 16, v114
	v_and_b32_e32 v151, 0xffff0000, v114
	v_lshlrev_b32_e32 v160, 16, v115
	v_and_b32_e32 v161, 0xffff0000, v115
	v_lshlrev_b32_e32 v162, 16, v116
	v_and_b32_e32 v163, 0xffff0000, v116
	v_lshlrev_b32_e32 v164, 16, v117
	v_and_b32_e32 v165, 0xffff0000, v117
	v_mul_f32_e32 v0, 0xbfb8aa3b, v0
	v_mul_f32_e32 v151, 0xbfb8aa3b, v151
	v_mul_f32_e32 v160, 0xbfb8aa3b, v160
	v_mul_f32_e32 v161, 0xbfb8aa3b, v161
	v_mul_f32_e32 v162, 0xbfb8aa3b, v162
	v_mul_f32_e32 v163, 0xbfb8aa3b, v163
	v_mul_f32_e32 v164, 0xbfb8aa3b, v164
	v_mul_f32_e32 v165, 0xbfb8aa3b, v165
	v_exp_f32_e32 v0, v0
	v_exp_f32_e32 v151, v151
	v_exp_f32_e32 v160, v160
	v_exp_f32_e32 v161, v161
	v_exp_f32_e32 v162, v162
	v_exp_f32_e32 v163, v163
	v_exp_f32_e32 v164, v164
	v_exp_f32_e32 v165, v165
	v_add_f32_e32 v0, 1.0, v0
	v_add_f32_e32 v151, 1.0, v151
	v_add_f32_e32 v160, 1.0, v160
	v_add_f32_e32 v161, 1.0, v161
	v_add_f32_e32 v162, 1.0, v162
	v_add_f32_e32 v163, 1.0, v163
	v_add_f32_e32 v164, 1.0, v164
	v_add_f32_e32 v165, 1.0, v165
	v_rcp_f32_e32 v0, v0
	v_rcp_f32_e32 v151, v151
	v_rcp_f32_e32 v160, v160
	v_rcp_f32_e32 v161, v161
	v_rcp_f32_e32 v162, v162
	v_rcp_f32_e32 v163, v163
	v_rcp_f32_e32 v164, v164
	v_rcp_f32_e32 v165, v165
	v_lshlrev_b32_e32 v166, 16, v118
	v_and_b32_e32 v118, 0xffff0000, v118
	v_lshlrev_b32_e32 v167, 16, v119
	v_and_b32_e32 v119, 0xffff0000, v119
	v_lshlrev_b32_e32 v170, 16, v120
	v_and_b32_e32 v120, 0xffff0000, v120
	v_lshlrev_b32_e32 v171, 16, v121
	v_and_b32_e32 v121, 0xffff0000, v121
	v_fmac_f32_e32 v166, v54, v0
	v_fmac_f32_e32 v118, v55, v151
	v_fmac_f32_e32 v167, v56, v160
	v_fmac_f32_e32 v119, v57, v161
	v_fmac_f32_e32 v170, v50, v162
	v_fmac_f32_e32 v120, v51, v163
	v_fmac_f32_e32 v171, v52, v164
	v_fmac_f32_e32 v121, v53, v165
	v_cvt_pk_bf16_f32 v118, v166, v118
	v_cvt_pk_bf16_f32 v119, v167, v119
	v_cvt_pk_bf16_f32 v120, v170, v120
	v_cvt_pk_bf16_f32 v121, v171, v121
	global_store_dwordx4 v[176:177], v[118:121], off offset:256
	s_waitcnt vmcnt(17)
	v_lshlrev_b32_e32 v0, 16, v106
	v_and_b32_e32 v151, 0xffff0000, v106
	v_lshlrev_b32_e32 v160, 16, v107
	v_and_b32_e32 v161, 0xffff0000, v107
	v_lshlrev_b32_e32 v162, 16, v108
	v_and_b32_e32 v163, 0xffff0000, v108
	v_lshlrev_b32_e32 v164, 16, v109
	v_and_b32_e32 v165, 0xffff0000, v109
	v_mul_f32_e32 v0, 0xbfb8aa3b, v0
	v_mul_f32_e32 v151, 0xbfb8aa3b, v151
	v_mul_f32_e32 v160, 0xbfb8aa3b, v160
	v_mul_f32_e32 v161, 0xbfb8aa3b, v161
	v_mul_f32_e32 v162, 0xbfb8aa3b, v162
	v_mul_f32_e32 v163, 0xbfb8aa3b, v163
	v_mul_f32_e32 v164, 0xbfb8aa3b, v164
	v_mul_f32_e32 v165, 0xbfb8aa3b, v165
	v_exp_f32_e32 v0, v0
	v_exp_f32_e32 v151, v151
	v_exp_f32_e32 v160, v160
	v_exp_f32_e32 v161, v161
	v_exp_f32_e32 v162, v162
	v_exp_f32_e32 v163, v163
	v_exp_f32_e32 v164, v164
	v_exp_f32_e32 v165, v165
	v_add_f32_e32 v0, 1.0, v0
	v_add_f32_e32 v151, 1.0, v151
	v_add_f32_e32 v160, 1.0, v160
	v_add_f32_e32 v161, 1.0, v161
	v_add_f32_e32 v162, 1.0, v162
	v_add_f32_e32 v163, 1.0, v163
	v_add_f32_e32 v164, 1.0, v164
	v_add_f32_e32 v165, 1.0, v165
	v_rcp_f32_e32 v0, v0
	v_rcp_f32_e32 v151, v151
	v_rcp_f32_e32 v160, v160
	v_rcp_f32_e32 v161, v161
	v_rcp_f32_e32 v162, v162
	v_rcp_f32_e32 v163, v163
	v_rcp_f32_e32 v164, v164
	v_rcp_f32_e32 v165, v165
	v_lshlrev_b32_e32 v166, 16, v110
	v_and_b32_e32 v110, 0xffff0000, v110
	v_lshlrev_b32_e32 v167, 16, v111
	v_and_b32_e32 v111, 0xffff0000, v111
	v_lshlrev_b32_e32 v170, 16, v112
	v_and_b32_e32 v112, 0xffff0000, v112
	v_lshlrev_b32_e32 v171, 16, v113
	v_and_b32_e32 v113, 0xffff0000, v113
	v_fmac_f32_e32 v166, v46, v0
	v_fmac_f32_e32 v110, v47, v151
	v_fmac_f32_e32 v167, v48, v160
	v_fmac_f32_e32 v111, v49, v161
	v_fmac_f32_e32 v170, v42, v162
	v_fmac_f32_e32 v112, v43, v163
	v_fmac_f32_e32 v171, v44, v164
	v_fmac_f32_e32 v113, v45, v165
	v_cvt_pk_bf16_f32 v110, v166, v110
	v_cvt_pk_bf16_f32 v111, v167, v111
	v_cvt_pk_bf16_f32 v112, v170, v112
	v_cvt_pk_bf16_f32 v113, v171, v113
	v_or_b32_e32 v176, 144, v150
	v_mov_b32_e32 v177, 0
	v_lshlrev_b64 v[176:177], 12, v[176:177]
	v_lshl_add_u64 v[176:177], s[10:11], 0, v[176:177]
	v_lshl_add_u64 v[176:177], v[176:177], 0, v[146:147]
	global_store_dwordx4 v[176:177], v[110:113], off
	s_waitcnt vmcnt(15)
	v_lshlrev_b32_e32 v0, 16, v98
	v_and_b32_e32 v151, 0xffff0000, v98
	v_lshlrev_b32_e32 v160, 16, v99
	v_and_b32_e32 v161, 0xffff0000, v99
	v_lshlrev_b32_e32 v162, 16, v100
	v_and_b32_e32 v163, 0xffff0000, v100
	v_lshlrev_b32_e32 v164, 16, v101
	v_and_b32_e32 v165, 0xffff0000, v101
	v_mul_f32_e32 v0, 0xbfb8aa3b, v0
	v_mul_f32_e32 v151, 0xbfb8aa3b, v151
	v_mul_f32_e32 v160, 0xbfb8aa3b, v160
	v_mul_f32_e32 v161, 0xbfb8aa3b, v161
	v_mul_f32_e32 v162, 0xbfb8aa3b, v162
	v_mul_f32_e32 v163, 0xbfb8aa3b, v163
	v_mul_f32_e32 v164, 0xbfb8aa3b, v164
	v_mul_f32_e32 v165, 0xbfb8aa3b, v165
	v_exp_f32_e32 v0, v0
	v_exp_f32_e32 v151, v151
	v_exp_f32_e32 v160, v160
	v_exp_f32_e32 v161, v161
	v_exp_f32_e32 v162, v162
	v_exp_f32_e32 v163, v163
	v_exp_f32_e32 v164, v164
	v_exp_f32_e32 v165, v165
	v_add_f32_e32 v0, 1.0, v0
	v_add_f32_e32 v151, 1.0, v151
	v_add_f32_e32 v160, 1.0, v160
	v_add_f32_e32 v161, 1.0, v161
	v_add_f32_e32 v162, 1.0, v162
	v_add_f32_e32 v163, 1.0, v163
	v_add_f32_e32 v164, 1.0, v164
	v_add_f32_e32 v165, 1.0, v165
	v_rcp_f32_e32 v0, v0
	v_rcp_f32_e32 v151, v151
	v_rcp_f32_e32 v160, v160
	v_rcp_f32_e32 v161, v161
	v_rcp_f32_e32 v162, v162
	v_rcp_f32_e32 v163, v163
	v_rcp_f32_e32 v164, v164
	v_rcp_f32_e32 v165, v165
	v_lshlrev_b32_e32 v166, 16, v102
	v_and_b32_e32 v102, 0xffff0000, v102
	v_lshlrev_b32_e32 v167, 16, v103
	v_and_b32_e32 v103, 0xffff0000, v103
	v_lshlrev_b32_e32 v170, 16, v104
	v_and_b32_e32 v104, 0xffff0000, v104
	v_lshlrev_b32_e32 v171, 16, v105
	v_and_b32_e32 v105, 0xffff0000, v105
	v_fmac_f32_e32 v166, v38, v0
	v_fmac_f32_e32 v102, v39, v151
	v_fmac_f32_e32 v167, v40, v160
	v_fmac_f32_e32 v103, v41, v161
	v_fmac_f32_e32 v170, v34, v162
	v_fmac_f32_e32 v104, v35, v163
	v_fmac_f32_e32 v171, v36, v164
	v_fmac_f32_e32 v105, v37, v165
	v_cvt_pk_bf16_f32 v102, v166, v102
	v_cvt_pk_bf16_f32 v103, v167, v103
	v_cvt_pk_bf16_f32 v104, v170, v104
	v_cvt_pk_bf16_f32 v105, v171, v105
	global_store_dwordx4 v[176:177], v[102:105], off offset:256
	s_waitcnt vmcnt(13)
	v_lshlrev_b32_e32 v0, 16, v90
	v_and_b32_e32 v151, 0xffff0000, v90
	v_lshlrev_b32_e32 v160, 16, v91
	v_and_b32_e32 v161, 0xffff0000, v91
	v_lshlrev_b32_e32 v162, 16, v92
	v_and_b32_e32 v163, 0xffff0000, v92
	v_lshlrev_b32_e32 v164, 16, v93
	v_and_b32_e32 v165, 0xffff0000, v93
	v_mul_f32_e32 v0, 0xbfb8aa3b, v0
	v_mul_f32_e32 v151, 0xbfb8aa3b, v151
	v_mul_f32_e32 v160, 0xbfb8aa3b, v160
	v_mul_f32_e32 v161, 0xbfb8aa3b, v161
	v_mul_f32_e32 v162, 0xbfb8aa3b, v162
	v_mul_f32_e32 v163, 0xbfb8aa3b, v163
	v_mul_f32_e32 v164, 0xbfb8aa3b, v164
	v_mul_f32_e32 v165, 0xbfb8aa3b, v165
	v_exp_f32_e32 v0, v0
	v_exp_f32_e32 v151, v151
	v_exp_f32_e32 v160, v160
	v_exp_f32_e32 v161, v161
	v_exp_f32_e32 v162, v162
	v_exp_f32_e32 v163, v163
	v_exp_f32_e32 v164, v164
	v_exp_f32_e32 v165, v165
	v_add_f32_e32 v0, 1.0, v0
	v_add_f32_e32 v151, 1.0, v151
	v_add_f32_e32 v160, 1.0, v160
	v_add_f32_e32 v161, 1.0, v161
	v_add_f32_e32 v162, 1.0, v162
	v_add_f32_e32 v163, 1.0, v163
	v_add_f32_e32 v164, 1.0, v164
	v_add_f32_e32 v165, 1.0, v165
	v_rcp_f32_e32 v0, v0
	v_rcp_f32_e32 v151, v151
	v_rcp_f32_e32 v160, v160
	v_rcp_f32_e32 v161, v161
	v_rcp_f32_e32 v162, v162
	v_rcp_f32_e32 v163, v163
	v_rcp_f32_e32 v164, v164
	v_rcp_f32_e32 v165, v165
	v_lshlrev_b32_e32 v166, 16, v94
	v_and_b32_e32 v94, 0xffff0000, v94
	v_lshlrev_b32_e32 v167, 16, v95
	v_and_b32_e32 v95, 0xffff0000, v95
	v_lshlrev_b32_e32 v170, 16, v96
	v_and_b32_e32 v96, 0xffff0000, v96
	v_lshlrev_b32_e32 v171, 16, v97
	v_and_b32_e32 v97, 0xffff0000, v97
	v_fmac_f32_e32 v166, v30, v0
	v_fmac_f32_e32 v94, v31, v151
	v_fmac_f32_e32 v167, v32, v160
	v_fmac_f32_e32 v95, v33, v161
	v_fmac_f32_e32 v170, v26, v162
	v_fmac_f32_e32 v96, v27, v163
	v_fmac_f32_e32 v171, v28, v164
	v_fmac_f32_e32 v97, v29, v165
	v_cvt_pk_bf16_f32 v94, v166, v94
	v_cvt_pk_bf16_f32 v95, v167, v95
	v_cvt_pk_bf16_f32 v96, v170, v96
	v_cvt_pk_bf16_f32 v97, v171, v97
	v_or_b32_e32 v176, 160, v150
	v_mov_b32_e32 v177, 0
	v_lshlrev_b64 v[176:177], 12, v[176:177]
	v_lshl_add_u64 v[176:177], s[10:11], 0, v[176:177]
	v_lshl_add_u64 v[176:177], v[176:177], 0, v[146:147]
	global_store_dwordx4 v[176:177], v[94:97], off
	s_waitcnt vmcnt(11)
	v_lshlrev_b32_e32 v0, 16, v82
	v_and_b32_e32 v151, 0xffff0000, v82
	v_lshlrev_b32_e32 v160, 16, v83
	v_and_b32_e32 v161, 0xffff0000, v83
	v_lshlrev_b32_e32 v162, 16, v84
	v_and_b32_e32 v163, 0xffff0000, v84
	v_lshlrev_b32_e32 v164, 16, v85
	v_and_b32_e32 v165, 0xffff0000, v85
	v_mul_f32_e32 v0, 0xbfb8aa3b, v0
	v_mul_f32_e32 v151, 0xbfb8aa3b, v151
	v_mul_f32_e32 v160, 0xbfb8aa3b, v160
	v_mul_f32_e32 v161, 0xbfb8aa3b, v161
	v_mul_f32_e32 v162, 0xbfb8aa3b, v162
	v_mul_f32_e32 v163, 0xbfb8aa3b, v163
	v_mul_f32_e32 v164, 0xbfb8aa3b, v164
	v_mul_f32_e32 v165, 0xbfb8aa3b, v165
	v_exp_f32_e32 v0, v0
	v_exp_f32_e32 v151, v151
	v_exp_f32_e32 v160, v160
	v_exp_f32_e32 v161, v161
	v_exp_f32_e32 v162, v162
	v_exp_f32_e32 v163, v163
	v_exp_f32_e32 v164, v164
	v_exp_f32_e32 v165, v165
	v_add_f32_e32 v0, 1.0, v0
	v_add_f32_e32 v151, 1.0, v151
	v_add_f32_e32 v160, 1.0, v160
	v_add_f32_e32 v161, 1.0, v161
	v_add_f32_e32 v162, 1.0, v162
	v_add_f32_e32 v163, 1.0, v163
	v_add_f32_e32 v164, 1.0, v164
	v_add_f32_e32 v165, 1.0, v165
	v_rcp_f32_e32 v0, v0
	v_rcp_f32_e32 v151, v151
	v_rcp_f32_e32 v160, v160
	v_rcp_f32_e32 v161, v161
	v_rcp_f32_e32 v162, v162
	v_rcp_f32_e32 v163, v163
	v_rcp_f32_e32 v164, v164
	v_rcp_f32_e32 v165, v165
	v_lshlrev_b32_e32 v166, 16, v86
	v_and_b32_e32 v86, 0xffff0000, v86
	v_lshlrev_b32_e32 v167, 16, v87
	v_and_b32_e32 v87, 0xffff0000, v87
	v_lshlrev_b32_e32 v170, 16, v88
	v_and_b32_e32 v88, 0xffff0000, v88
	v_lshlrev_b32_e32 v171, 16, v89
	v_and_b32_e32 v89, 0xffff0000, v89
	v_fmac_f32_e32 v166, v22, v0
	v_fmac_f32_e32 v86, v23, v151
	v_fmac_f32_e32 v167, v24, v160
	v_fmac_f32_e32 v87, v25, v161
	v_fmac_f32_e32 v170, v18, v162
	v_fmac_f32_e32 v88, v19, v163
	v_fmac_f32_e32 v171, v20, v164
	v_fmac_f32_e32 v89, v21, v165
	v_cvt_pk_bf16_f32 v86, v166, v86
	v_cvt_pk_bf16_f32 v87, v167, v87
	v_cvt_pk_bf16_f32 v88, v170, v88
	v_cvt_pk_bf16_f32 v89, v171, v89
	global_store_dwordx4 v[176:177], v[86:89], off offset:256
	s_waitcnt vmcnt(9)
	v_lshlrev_b32_e32 v0, 16, v74
	v_and_b32_e32 v151, 0xffff0000, v74
	v_lshlrev_b32_e32 v160, 16, v75
	v_and_b32_e32 v161, 0xffff0000, v75
	v_lshlrev_b32_e32 v162, 16, v76
	v_and_b32_e32 v163, 0xffff0000, v76
	v_lshlrev_b32_e32 v164, 16, v77
	v_and_b32_e32 v165, 0xffff0000, v77
	v_mul_f32_e32 v0, 0xbfb8aa3b, v0
	v_mul_f32_e32 v151, 0xbfb8aa3b, v151
	v_mul_f32_e32 v160, 0xbfb8aa3b, v160
	v_mul_f32_e32 v161, 0xbfb8aa3b, v161
	v_mul_f32_e32 v162, 0xbfb8aa3b, v162
	v_mul_f32_e32 v163, 0xbfb8aa3b, v163
	v_mul_f32_e32 v164, 0xbfb8aa3b, v164
	v_mul_f32_e32 v165, 0xbfb8aa3b, v165
	v_exp_f32_e32 v0, v0
	v_exp_f32_e32 v151, v151
	v_exp_f32_e32 v160, v160
	v_exp_f32_e32 v161, v161
	v_exp_f32_e32 v162, v162
	v_exp_f32_e32 v163, v163
	v_exp_f32_e32 v164, v164
	v_exp_f32_e32 v165, v165
	v_add_f32_e32 v0, 1.0, v0
	v_add_f32_e32 v151, 1.0, v151
	v_add_f32_e32 v160, 1.0, v160
	v_add_f32_e32 v161, 1.0, v161
	v_add_f32_e32 v162, 1.0, v162
	v_add_f32_e32 v163, 1.0, v163
	v_add_f32_e32 v164, 1.0, v164
	v_add_f32_e32 v165, 1.0, v165
	v_rcp_f32_e32 v0, v0
	v_rcp_f32_e32 v151, v151
	v_rcp_f32_e32 v160, v160
	v_rcp_f32_e32 v161, v161
	v_rcp_f32_e32 v162, v162
	v_rcp_f32_e32 v163, v163
	v_rcp_f32_e32 v164, v164
	v_rcp_f32_e32 v165, v165
	v_lshlrev_b32_e32 v166, 16, v78
	v_and_b32_e32 v78, 0xffff0000, v78
	v_lshlrev_b32_e32 v167, 16, v79
	v_and_b32_e32 v79, 0xffff0000, v79
	v_lshlrev_b32_e32 v170, 16, v80
	v_and_b32_e32 v80, 0xffff0000, v80
	v_lshlrev_b32_e32 v171, 16, v81
	v_and_b32_e32 v81, 0xffff0000, v81
	v_fmac_f32_e32 v166, v14, v0
	v_fmac_f32_e32 v78, v15, v151
	v_fmac_f32_e32 v167, v16, v160
	v_fmac_f32_e32 v79, v17, v161
	v_fmac_f32_e32 v170, v10, v162
	v_fmac_f32_e32 v80, v11, v163
	v_fmac_f32_e32 v171, v12, v164
	v_fmac_f32_e32 v81, v13, v165
	v_cvt_pk_bf16_f32 v78, v166, v78
	v_cvt_pk_bf16_f32 v79, v167, v79
	v_cvt_pk_bf16_f32 v80, v170, v80
	v_cvt_pk_bf16_f32 v81, v171, v81
	v_or_b32_e32 v176, 176, v150
	v_mov_b32_e32 v177, 0
	v_lshlrev_b64 v[176:177], 12, v[176:177]
	v_lshl_add_u64 v[176:177], s[10:11], 0, v[176:177]
	v_lshl_add_u64 v[176:177], v[176:177], 0, v[146:147]
	global_store_dwordx4 v[176:177], v[78:81], off
	s_waitcnt vmcnt(7)
	v_lshlrev_b32_e32 v0, 16, v66
	v_and_b32_e32 v151, 0xffff0000, v66
	v_lshlrev_b32_e32 v160, 16, v67
	v_and_b32_e32 v161, 0xffff0000, v67
	v_lshlrev_b32_e32 v162, 16, v68
	v_and_b32_e32 v163, 0xffff0000, v68
	v_lshlrev_b32_e32 v164, 16, v69
	v_and_b32_e32 v165, 0xffff0000, v69
	v_mul_f32_e32 v0, 0xbfb8aa3b, v0
	v_mul_f32_e32 v151, 0xbfb8aa3b, v151
	v_mul_f32_e32 v160, 0xbfb8aa3b, v160
	v_mul_f32_e32 v161, 0xbfb8aa3b, v161
	v_mul_f32_e32 v162, 0xbfb8aa3b, v162
	v_mul_f32_e32 v163, 0xbfb8aa3b, v163
	v_mul_f32_e32 v164, 0xbfb8aa3b, v164
	v_mul_f32_e32 v165, 0xbfb8aa3b, v165
	v_exp_f32_e32 v0, v0
	v_exp_f32_e32 v151, v151
	v_exp_f32_e32 v160, v160
	v_exp_f32_e32 v161, v161
	v_exp_f32_e32 v162, v162
	v_exp_f32_e32 v163, v163
	v_exp_f32_e32 v164, v164
	v_exp_f32_e32 v165, v165
	v_add_f32_e32 v0, 1.0, v0
	v_add_f32_e32 v151, 1.0, v151
	v_add_f32_e32 v160, 1.0, v160
	v_add_f32_e32 v161, 1.0, v161
	v_add_f32_e32 v162, 1.0, v162
	v_add_f32_e32 v163, 1.0, v163
	v_add_f32_e32 v164, 1.0, v164
	v_add_f32_e32 v165, 1.0, v165
	v_rcp_f32_e32 v0, v0
	v_rcp_f32_e32 v151, v151
	v_rcp_f32_e32 v160, v160
	v_rcp_f32_e32 v161, v161
	v_rcp_f32_e32 v162, v162
	v_rcp_f32_e32 v163, v163
	v_rcp_f32_e32 v164, v164
	v_rcp_f32_e32 v165, v165
	v_lshlrev_b32_e32 v166, 16, v70
	v_and_b32_e32 v70, 0xffff0000, v70
	v_lshlrev_b32_e32 v167, 16, v71
	v_and_b32_e32 v71, 0xffff0000, v71
	v_lshlrev_b32_e32 v170, 16, v72
	v_and_b32_e32 v72, 0xffff0000, v72
	v_lshlrev_b32_e32 v171, 16, v73
	v_and_b32_e32 v73, 0xffff0000, v73
	v_fmac_f32_e32 v166, v6, v0
	v_fmac_f32_e32 v70, v7, v151
	v_fmac_f32_e32 v167, v8, v160
	v_fmac_f32_e32 v71, v9, v161
	v_fmac_f32_e32 v170, v2, v162
	v_fmac_f32_e32 v72, v3, v163
	v_fmac_f32_e32 v171, v4, v164
	v_fmac_f32_e32 v73, v5, v165
	v_cvt_pk_bf16_f32 v70, v166, v70
	v_cvt_pk_bf16_f32 v71, v167, v71
	v_cvt_pk_bf16_f32 v72, v170, v72
	v_cvt_pk_bf16_f32 v73, v171, v73
	global_store_dwordx4 v[176:177], v[70:73], off offset:256
	s_andn2_b64 vcc, exec, s[4:5]
	s_mov_b64 s[4:5], -1
	s_cbranch_vccnz .LBB0_1145
	s_andn2_b64 vcc, exec, s[8:9]
	s_cbranch_vccnz .LBB0_1144
	s_barrier
	s_branch .LBB0_1144

.LBB0_1231:
	v_lshl_add_u32 v150, s34, 8, v1
	v_lshl_or_b32 v148, s56, 8, v153
	v_ashrrev_i32_e32 v149, 31, v148
	v_mov_b32_e32 v146, v150
	v_mov_b32_e32 v147, 0
	v_lshlrev_b64 v[146:147], 11, v[146:147]
	v_lshl_add_u64 v[146:147], v[146:147], 0, v[148:149]
	v_lshl_add_u64 v[158:159], v[146:147], 2, s[6:7]
	global_load_dwordx4 v[170:173], v[158:159], off nt
	global_load_dwordx4 v[174:177], v[158:159], off offset:16 nt
	global_load_dwordx4 v[178:181], v[158:159], off offset:512 nt
	global_load_dwordx4 v[182:185], v[158:159], off offset:528 nt
	v_or_b32_e32 v146, 16, v150
	v_mov_b32_e32 v147, 0
	v_lshlrev_b64 v[146:147], 11, v[146:147]
	v_lshl_add_u64 v[146:147], v[146:147], 0, v[148:149]
	v_lshl_add_u64 v[158:159], v[146:147], 2, s[6:7]
	global_load_dwordx4 v[186:189], v[158:159], off nt
	global_load_dwordx4 v[190:193], v[158:159], off offset:16 nt
	global_load_dwordx4 v[194:197], v[158:159], off offset:512 nt
	global_load_dwordx4 v[198:201], v[158:159], off offset:528 nt
	v_or_b32_e32 v146, 32, v150
	v_mov_b32_e32 v147, 0
	v_lshlrev_b64 v[146:147], 11, v[146:147]
	v_lshl_add_u64 v[146:147], v[146:147], 0, v[148:149]
	v_lshl_add_u64 v[158:159], v[146:147], 2, s[6:7]
	global_load_dwordx4 v[202:205], v[158:159], off nt
	global_load_dwordx4 v[206:209], v[158:159], off offset:16 nt
	global_load_dwordx4 v[210:213], v[158:159], off offset:512 nt
	global_load_dwordx4 v[214:217], v[158:159], off offset:528 nt
	v_or_b32_e32 v146, 48, v150
	v_mov_b32_e32 v147, 0
	v_lshlrev_b64 v[146:147], 11, v[146:147]
	v_lshl_add_u64 v[146:147], v[146:147], 0, v[148:149]
	v_lshl_add_u64 v[158:159], v[146:147], 2, s[6:7]
	global_load_dwordx4 v[222:225], v[158:159], off nt
	global_load_dwordx4 v[226:229], v[158:159], off offset:16 nt
	global_load_dwordx4 v[230:233], v[158:159], off offset:512 nt
	global_load_dwordx4 v[234:237], v[158:159], off offset:528 nt
	s_waitcnt vmcnt(14)
	v_pk_add_f32 v[126:127], v[126:127], v[170:171]
	v_pk_add_f32 v[128:129], v[128:129], v[172:173]
	v_pk_add_f32 v[122:123], v[122:123], v[174:175]
	v_pk_add_f32 v[124:125], v[124:125], v[176:177]
	v_cvt_pk_bf16_f32 v170, v126, v127
	v_cvt_pk_bf16_f32 v171, v128, v129
	v_cvt_pk_bf16_f32 v172, v122, v123
	v_cvt_pk_bf16_f32 v173, v124, v125
	v_mov_b32_e32 v160, v150
	v_mov_b32_e32 v161, 0
	v_lshlrev_b64 v[160:161], 11, v[160:161]
	v_lshl_add_u64 v[160:161], v[160:161], 0, v[148:149]
	v_lshl_add_u64 v[160:161], v[160:161], 1, s[10:11]
	global_store_dwordx4 v[160:161], v[170:173], off
	v_or_b32_e32 v146, 128, v150
	v_mov_b32_e32 v147, 0
	v_lshlrev_b64 v[146:147], 11, v[146:147]
	v_lshl_add_u64 v[146:147], v[146:147], 0, v[148:149]
	v_lshl_add_u64 v[158:159], v[146:147], 2, s[6:7]
	global_load_dwordx4 v[126:129], v[158:159], off nt
	global_load_dwordx4 v[122:125], v[158:159], off offset:16 nt
	s_waitcnt vmcnt(15)
	v_pk_add_f32 v[118:119], v[118:119], v[178:179]
	v_pk_add_f32 v[120:121], v[120:121], v[180:181]
	v_pk_add_f32 v[114:115], v[114:115], v[182:183]
	v_pk_add_f32 v[116:117], v[116:117], v[184:185]
	v_cvt_pk_bf16_f32 v178, v118, v119
	v_cvt_pk_bf16_f32 v179, v120, v121
	v_cvt_pk_bf16_f32 v180, v114, v115
	v_cvt_pk_bf16_f32 v181, v116, v117
	global_store_dwordx4 v[160:161], v[178:181], off offset:256
	global_load_dwordx4 v[118:121], v[158:159], off offset:512 nt
	global_load_dwordx4 v[114:117], v[158:159], off offset:528 nt
	s_waitcnt vmcnt(16)
	v_pk_add_f32 v[110:111], v[110:111], v[186:187]
	v_pk_add_f32 v[112:113], v[112:113], v[188:189]
	v_pk_add_f32 v[106:107], v[106:107], v[190:191]
	v_pk_add_f32 v[108:109], v[108:109], v[192:193]
	v_cvt_pk_bf16_f32 v186, v110, v111
	v_cvt_pk_bf16_f32 v187, v112, v113
	v_cvt_pk_bf16_f32 v188, v106, v107
	v_cvt_pk_bf16_f32 v189, v108, v109
	v_or_b32_e32 v160, 16, v150
	v_mov_b32_e32 v161, 0
	v_lshlrev_b64 v[160:161], 11, v[160:161]
	v_lshl_add_u64 v[160:161], v[160:161], 0, v[148:149]
	v_lshl_add_u64 v[160:161], v[160:161], 1, s[10:11]
	global_store_dwordx4 v[160:161], v[186:189], off
	v_or_b32_e32 v146, 144, v150
	v_mov_b32_e32 v147, 0
	v_lshlrev_b64 v[146:147], 11, v[146:147]
	v_lshl_add_u64 v[146:147], v[146:147], 0, v[148:149]
	v_lshl_add_u64 v[158:159], v[146:147], 2, s[6:7]
	global_load_dwordx4 v[110:113], v[158:159], off nt
	global_load_dwordx4 v[106:109], v[158:159], off offset:16 nt
	s_waitcnt vmcnt(17)
	v_pk_add_f32 v[102:103], v[102:103], v[194:195]
	v_pk_add_f32 v[104:105], v[104:105], v[196:197]
	v_pk_add_f32 v[98:99], v[98:99], v[198:199]
	v_pk_add_f32 v[100:101], v[100:101], v[200:201]
	v_cvt_pk_bf16_f32 v194, v102, v103
	v_cvt_pk_bf16_f32 v195, v104, v105
	v_cvt_pk_bf16_f32 v196, v98, v99
	v_cvt_pk_bf16_f32 v197, v100, v101
	global_store_dwordx4 v[160:161], v[194:197], off offset:256
	global_load_dwordx4 v[102:105], v[158:159], off offset:512 nt
	global_load_dwordx4 v[98:101], v[158:159], off offset:528 nt
	s_waitcnt vmcnt(18)
	v_pk_add_f32 v[94:95], v[94:95], v[202:203]
	v_pk_add_f32 v[96:97], v[96:97], v[204:205]
	v_pk_add_f32 v[90:91], v[90:91], v[206:207]
	v_pk_add_f32 v[92:93], v[92:93], v[208:209]
	v_cvt_pk_bf16_f32 v202, v94, v95
	v_cvt_pk_bf16_f32 v203, v96, v97
	v_cvt_pk_bf16_f32 v204, v90, v91
	v_cvt_pk_bf16_f32 v205, v92, v93
	v_or_b32_e32 v160, 32, v150
	v_mov_b32_e32 v161, 0
	v_lshlrev_b64 v[160:161], 11, v[160:161]
	v_lshl_add_u64 v[160:161], v[160:161], 0, v[148:149]
	v_lshl_add_u64 v[160:161], v[160:161], 1, s[10:11]
	global_store_dwordx4 v[160:161], v[202:205], off
	v_or_b32_e32 v146, 160, v150
	v_mov_b32_e32 v147, 0
	v_lshlrev_b64 v[146:147], 11, v[146:147]
	v_lshl_add_u64 v[146:147], v[146:147], 0, v[148:149]
	v_lshl_add_u64 v[158:159], v[146:147], 2, s[6:7]
	global_load_dwordx4 v[94:97], v[158:159], off nt
	global_load_dwordx4 v[90:93], v[158:159], off offset:16 nt
	s_waitcnt vmcnt(19)
	v_pk_add_f32 v[86:87], v[86:87], v[210:211]
	v_pk_add_f32 v[88:89], v[88:89], v[212:213]
	v_pk_add_f32 v[82:83], v[82:83], v[214:215]
	v_pk_add_f32 v[84:85], v[84:85], v[216:217]
	v_cvt_pk_bf16_f32 v210, v86, v87
	v_cvt_pk_bf16_f32 v211, v88, v89
	v_cvt_pk_bf16_f32 v212, v82, v83
	v_cvt_pk_bf16_f32 v213, v84, v85
	global_store_dwordx4 v[160:161], v[210:213], off offset:256
	global_load_dwordx4 v[86:89], v[158:159], off offset:512 nt
	global_load_dwordx4 v[82:85], v[158:159], off offset:528 nt
	s_waitcnt vmcnt(20)
	v_pk_add_f32 v[78:79], v[78:79], v[222:223]
	v_pk_add_f32 v[80:81], v[80:81], v[224:225]
	v_pk_add_f32 v[74:75], v[74:75], v[226:227]
	v_pk_add_f32 v[76:77], v[76:77], v[228:229]
	v_cvt_pk_bf16_f32 v222, v78, v79
	v_cvt_pk_bf16_f32 v223, v80, v81
	v_cvt_pk_bf16_f32 v224, v74, v75
	v_cvt_pk_bf16_f32 v225, v76, v77
	v_or_b32_e32 v160, 48, v150
	v_mov_b32_e32 v161, 0
	v_lshlrev_b64 v[160:161], 11, v[160:161]
	v_lshl_add_u64 v[160:161], v[160:161], 0, v[148:149]
	v_lshl_add_u64 v[160:161], v[160:161], 1, s[10:11]
	global_store_dwordx4 v[160:161], v[222:225], off
	v_or_b32_e32 v146, 176, v150
	v_mov_b32_e32 v147, 0
	v_lshlrev_b64 v[146:147], 11, v[146:147]
	v_lshl_add_u64 v[146:147], v[146:147], 0, v[148:149]
	v_lshl_add_u64 v[158:159], v[146:147], 2, s[6:7]
	global_load_dwordx4 v[78:81], v[158:159], off nt
	global_load_dwordx4 v[74:77], v[158:159], off offset:16 nt
	s_waitcnt vmcnt(21)
	v_pk_add_f32 v[70:71], v[70:71], v[230:231]
	v_pk_add_f32 v[72:73], v[72:73], v[232:233]
	v_pk_add_f32 v[66:67], v[66:67], v[234:235]
	v_pk_add_f32 v[68:69], v[68:69], v[236:237]
	v_cvt_pk_bf16_f32 v230, v70, v71
	v_cvt_pk_bf16_f32 v231, v72, v73
	v_cvt_pk_bf16_f32 v232, v66, v67
	v_cvt_pk_bf16_f32 v233, v68, v69
	global_store_dwordx4 v[160:161], v[230:233], off offset:256
	global_load_dwordx4 v[70:73], v[158:159], off offset:512 nt
	global_load_dwordx4 v[66:69], v[158:159], off offset:528 nt
	s_waitcnt vmcnt(21)
	v_pk_add_f32 v[62:63], v[62:63], v[126:127]
	v_pk_add_f32 v[64:65], v[64:65], v[128:129]
	v_pk_add_f32 v[58:59], v[58:59], v[122:123]
	v_pk_add_f32 v[60:61], v[60:61], v[124:125]
	v_cvt_pk_bf16_f32 v126, v62, v63
	v_cvt_pk_bf16_f32 v127, v64, v65
	v_cvt_pk_bf16_f32 v128, v58, v59
	v_cvt_pk_bf16_f32 v129, v60, v61
	v_or_b32_e32 v160, 128, v150
	v_mov_b32_e32 v161, 0
	v_lshlrev_b64 v[160:161], 11, v[160:161]
	v_lshl_add_u64 v[160:161], v[160:161], 0, v[148:149]
	v_lshl_add_u64 v[160:161], v[160:161], 1, s[10:11]
	global_store_dwordx4 v[160:161], v[126:129], off
	s_waitcnt vmcnt(19)
	v_pk_add_f32 v[54:55], v[54:55], v[118:119]
	v_pk_add_f32 v[56:57], v[56:57], v[120:121]
	v_pk_add_f32 v[50:51], v[50:51], v[114:115]
	v_pk_add_f32 v[52:53], v[52:53], v[116:117]
	v_cvt_pk_bf16_f32 v118, v54, v55
	v_cvt_pk_bf16_f32 v119, v56, v57
	v_cvt_pk_bf16_f32 v120, v50, v51
	v_cvt_pk_bf16_f32 v121, v52, v53
	global_store_dwordx4 v[160:161], v[118:121], off offset:256
	s_waitcnt vmcnt(17)
	v_pk_add_f32 v[46:47], v[46:47], v[110:111]
	v_pk_add_f32 v[48:49], v[48:49], v[112:113]
	v_pk_add_f32 v[42:43], v[42:43], v[106:107]
	v_pk_add_f32 v[44:45], v[44:45], v[108:109]
	v_cvt_pk_bf16_f32 v110, v46, v47
	v_cvt_pk_bf16_f32 v111, v48, v49
	v_cvt_pk_bf16_f32 v112, v42, v43
	v_cvt_pk_bf16_f32 v113, v44, v45
	v_or_b32_e32 v160, 144, v150
	v_mov_b32_e32 v161, 0
	v_lshlrev_b64 v[160:161], 11, v[160:161]
	v_lshl_add_u64 v[160:161], v[160:161], 0, v[148:149]
	v_lshl_add_u64 v[160:161], v[160:161], 1, s[10:11]
	global_store_dwordx4 v[160:161], v[110:113], off
	s_waitcnt vmcnt(15)
	v_pk_add_f32 v[38:39], v[38:39], v[102:103]
	v_pk_add_f32 v[40:41], v[40:41], v[104:105]
	v_pk_add_f32 v[34:35], v[34:35], v[98:99]
	v_pk_add_f32 v[36:37], v[36:37], v[100:101]
	v_cvt_pk_bf16_f32 v102, v38, v39
	v_cvt_pk_bf16_f32 v103, v40, v41
	v_cvt_pk_bf16_f32 v104, v34, v35
	v_cvt_pk_bf16_f32 v105, v36, v37
	global_store_dwordx4 v[160:161], v[102:105], off offset:256
	s_waitcnt vmcnt(13)
	v_pk_add_f32 v[30:31], v[30:31], v[94:95]
	v_pk_add_f32 v[32:33], v[32:33], v[96:97]
	v_pk_add_f32 v[26:27], v[26:27], v[90:91]
	v_pk_add_f32 v[28:29], v[28:29], v[92:93]
	v_cvt_pk_bf16_f32 v94, v30, v31
	v_cvt_pk_bf16_f32 v95, v32, v33
	v_cvt_pk_bf16_f32 v96, v26, v27
	v_cvt_pk_bf16_f32 v97, v28, v29
	v_or_b32_e32 v160, 160, v150
	v_mov_b32_e32 v161, 0
	v_lshlrev_b64 v[160:161], 11, v[160:161]
	v_lshl_add_u64 v[160:161], v[160:161], 0, v[148:149]
	v_lshl_add_u64 v[160:161], v[160:161], 1, s[10:11]
	global_store_dwordx4 v[160:161], v[94:97], off
	s_waitcnt vmcnt(11)
	v_pk_add_f32 v[22:23], v[22:23], v[86:87]
	v_pk_add_f32 v[24:25], v[24:25], v[88:89]
	v_pk_add_f32 v[18:19], v[18:19], v[82:83]
	v_pk_add_f32 v[20:21], v[20:21], v[84:85]
	v_cvt_pk_bf16_f32 v86, v22, v23
	v_cvt_pk_bf16_f32 v87, v24, v25
	v_cvt_pk_bf16_f32 v88, v18, v19
	v_cvt_pk_bf16_f32 v89, v20, v21
	global_store_dwordx4 v[160:161], v[86:89], off offset:256
	s_waitcnt vmcnt(9)
	v_pk_add_f32 v[14:15], v[14:15], v[78:79]
	v_pk_add_f32 v[16:17], v[16:17], v[80:81]
	v_pk_add_f32 v[10:11], v[10:11], v[74:75]
	v_pk_add_f32 v[12:13], v[12:13], v[76:77]
	v_cvt_pk_bf16_f32 v78, v14, v15
	v_cvt_pk_bf16_f32 v79, v16, v17
	v_cvt_pk_bf16_f32 v80, v10, v11
	v_cvt_pk_bf16_f32 v81, v12, v13
	v_or_b32_e32 v160, 176, v150
	v_mov_b32_e32 v161, 0
	v_lshlrev_b64 v[160:161], 11, v[160:161]
	v_lshl_add_u64 v[160:161], v[160:161], 0, v[148:149]
	v_lshl_add_u64 v[160:161], v[160:161], 1, s[10:11]
	global_store_dwordx4 v[160:161], v[78:81], off
	s_waitcnt vmcnt(7)
	v_pk_add_f32 v[6:7], v[6:7], v[70:71]
	v_pk_add_f32 v[8:9], v[8:9], v[72:73]
	v_pk_add_f32 v[2:3], v[2:3], v[66:67]
	v_pk_add_f32 v[4:5], v[4:5], v[68:69]
	v_cvt_pk_bf16_f32 v70, v6, v7
	v_cvt_pk_bf16_f32 v71, v8, v9
	v_cvt_pk_bf16_f32 v72, v2, v3
	v_cvt_pk_bf16_f32 v73, v4, v5
	global_store_dwordx4 v[160:161], v[70:73], off offset:256
	s_andn2_b64 vcc, exec, s[4:5]
	s_mov_b64 s[4:5], -1
	s_cbranch_vccnz .LBB0_1220
	s_andn2_b64 vcc, exec, s[8:9]
	s_cbranch_vccnz .LBB0_1219
	s_barrier
	s_branch .LBB0_1219
